# v048 + agent-scope (sc1, L1 bypass) on the fused kernel's touch-once residual loads
# speedup vs baseline: 1.0072x; 1.0072x over previous
.LBB3_141:
	s_mul_i32 s2, s41, 0x6000
	v_or_b32_e32 v98, s2, v206
	v_add_u32_e32 v250, 0x12000, v98
	ds_read_b128 v[98:101], v250 offset:8192
	v_cvt_pk_bf16_f32 v50, v50, v51
	v_cvt_pk_bf16_f32 v51, v52, v53
	v_cvt_pk_bf16_f32 v52, v54, v55
	v_cvt_pk_bf16_f32 v53, v56, v57
	ds_read_b128 v[54:57], v250 offset:9216
	v_cvt_pk_bf16_f32 v214, v82, v83
	v_cvt_pk_bf16_f32 v215, v84, v85
	ds_read_b128 v[82:85], v250 offset:13312
	s_waitcnt lgkmcnt(2)
	v_mfma_f32_32x32x16_bf16 v[114:129], v[98:101], v[50:53], 0
	ds_read_b128 v[98:101], v250 offset:12288
	v_cvt_pk_bf16_f32 v18, v18, v19
	v_cvt_pk_bf16_f32 v19, v20, v21
	v_cvt_pk_bf16_f32 v20, v22, v23
	v_cvt_pk_bf16_f32 v21, v24, v25
	v_cvt_pk_bf16_f32 v216, v86, v87
	v_cvt_pk_bf16_f32 v217, v88, v89
	v_cvt_pk_bf16_f32 v86, v10, v11
	s_waitcnt lgkmcnt(0)
	v_mfma_f32_32x32x16_bf16 v[98:113], v[98:101], v[50:53], 0
	v_cvt_pk_bf16_f32 v50, v58, v59
	v_cvt_pk_bf16_f32 v51, v60, v61
	v_cvt_pk_bf16_f32 v52, v62, v63
	v_cvt_pk_bf16_f32 v53, v64, v65
	ds_read_b128 v[58:61], v250 offset:10240
	v_cvt_pk_bf16_f32 v87, v12, v13
	v_cvt_pk_bf16_f32 v88, v14, v15
	v_mfma_f32_32x32x16_bf16 v[114:129], v[54:57], v[50:53], v[114:129]
	v_cvt_pk_bf16_f32 v2, v2, v3
	v_cvt_pk_bf16_f32 v3, v4, v5
	v_cvt_pk_bf16_f32 v4, v6, v7
	v_cvt_pk_bf16_f32 v5, v8, v9
	v_cvt_pk_bf16_f32 v6, v42, v43
	v_cvt_pk_bf16_f32 v7, v44, v45
	v_cvt_pk_bf16_f32 v8, v46, v47
	v_mfma_f32_32x32x16_bf16 v[98:113], v[82:85], v[50:53], v[98:113]
	ds_read_b128 v[22:25], v250 offset:14336
	ds_read_b128 v[50:53], v250 offset:11264
	ds_read_b128 v[10:13], v250
	v_cvt_pk_bf16_f32 v9, v48, v49
	v_cvt_pk_bf16_f32 v54, v90, v91
	v_cvt_pk_bf16_f32 v55, v92, v93
	v_cvt_pk_bf16_f32 v56, v94, v95
	v_cvt_pk_bf16_f32 v57, v96, v97
	s_waitcnt lgkmcnt(3)
	v_mfma_f32_32x32x16_bf16 v[114:129], v[58:61], v[18:21], v[114:129]
	v_cvt_pk_bf16_f32 v58, v34, v35
	v_cvt_pk_bf16_f32 v59, v36, v37
	ds_read_b128 v[34:37], v250 offset:15360
	v_cvt_pk_bf16_f32 v60, v38, v39
	v_cvt_pk_bf16_f32 v61, v40, v41
	v_cvt_pk_bf16_f32 v202, v66, v67
	v_cvt_pk_bf16_f32 v203, v68, v69
	s_waitcnt lgkmcnt(3)
	v_mfma_f32_32x32x16_bf16 v[98:113], v[22:25], v[18:21], v[98:113]
	v_cvt_pk_bf16_f32 v18, v26, v27
	v_cvt_pk_bf16_f32 v19, v28, v29
	v_cvt_pk_bf16_f32 v20, v30, v31
	v_cvt_pk_bf16_f32 v21, v32, v33
	v_cvt_pk_bf16_f32 v204, v70, v71
	v_cvt_pk_bf16_f32 v205, v72, v73
	v_cvt_pk_bf16_f32 v82, v74, v75
	s_waitcnt lgkmcnt(2)
	v_mfma_f32_32x32x16_bf16 v[114:129], v[50:53], v[18:21], v[114:129]
	v_cvt_pk_bf16_f32 v83, v76, v77
	v_cvt_pk_bf16_f32 v84, v78, v79
	v_cvt_pk_bf16_f32 v85, v80, v81
	s_lshl_b32 s2, s20, 6
	s_mov_b32 s41, 1
	s_mov_b64 s[20:21], 0
	s_nop 5
	v_max3_f32 v14, v114, s38, v115
	s_waitcnt lgkmcnt(0)
	v_mfma_f32_32x32x16_bf16 v[98:113], v[34:37], v[18:21], v[98:113]
	ds_read_b128 v[50:53], v250 offset:1024
	ds_read_b128 v[18:21], v250 offset:4096
	ds_read_b128 v[62:65], v250 offset:5120
	v_max3_f32 v14, v14, v116, v117
	v_max3_f32 v14, v14, v118, v119
	v_max3_f32 v14, v14, v120, v121
	v_max3_f32 v14, v14, v122, v123
	v_max3_f32 v14, v14, v124, v125
	v_max3_f32 v14, v14, v126, v127
	v_mfma_f32_32x32x16_bf16 v[34:49], v[214:217], v[10:13], 0
	v_max3_f32 v14, v14, v128, v129
	s_nop 0
	v_max3_f32 v14, v14, v98, v99
	v_max3_f32 v14, v14, v100, v101
	v_max3_f32 v14, v14, v102, v103
	v_max3_f32 v14, v14, v104, v105
	v_max3_f32 v14, v14, v106, v107
	v_max3_f32 v14, v14, v108, v109
	s_waitcnt lgkmcnt(1)
	v_mfma_f32_32x32x16_bf16 v[18:33], v[214:217], v[18:21], 0
	v_max3_f32 v14, v14, v110, v111
	v_max3_f32 v14, v14, v112, v113
	v_mov_b32_e32 v15, v14
	ds_read_b128 v[10:13], v250 offset:2048
	ds_read_b128 v[66:69], v250 offset:3072
	ds_read_b128 v[70:73], v250 offset:6144
	ds_read_b128 v[74:77], v250 offset:7168
	v_permlane32_swap_b32_e32 v14, v15
	v_max_f32_e32 v15, v15, v15
	v_mfma_f32_32x32x16_bf16 v[34:49], v[54:57], v[50:53], v[34:49]
	v_max_f32_e32 v14, v14, v14
	v_max_f32_e32 v14, v14, v15
	v_mul_f32_e32 v14, 0xbe38aa3b, v14
	v_fmamk_f32 v15, v114, 0x3e38aa3b, v14
	v_fmamk_f32 v50, v118, 0x3e38aa3b, v14
	v_exp_f32_e32 v50, v50
	v_fmamk_f32 v51, v119, 0x3e38aa3b, v14
	s_waitcnt lgkmcnt(4)
	v_mfma_f32_32x32x16_bf16 v[18:33], v[54:57], v[62:65], v[18:33]
	v_exp_f32_e32 v51, v51
	v_fmamk_f32 v52, v120, 0x3e38aa3b, v14
	v_exp_f32_e32 v52, v52
	v_fmamk_f32 v53, v121, 0x3e38aa3b, v14
	v_exp_f32_e32 v53, v53
	v_fmamk_f32 v109, v109, 0x3e38aa3b, v14
	s_waitcnt lgkmcnt(3)
	v_mfma_f32_32x32x16_bf16 v[34:49], v[58:61], v[10:13], v[34:49]
	v_exp_f32_e32 v10, v15
	v_fmamk_f32 v11, v115, 0x3e38aa3b, v14
	v_exp_f32_e32 v11, v11
	v_fmamk_f32 v12, v116, 0x3e38aa3b, v14
	v_exp_f32_e32 v12, v12
	v_fmamk_f32 v15, v117, 0x3e38aa3b, v14
	v_exp_f32_e32 v15, v15
	s_waitcnt lgkmcnt(1)
	v_mfma_f32_32x32x16_bf16 v[18:33], v[58:61], v[70:73], v[18:33]
	v_add_f32_e32 v13, 0, v10
	v_add_f32_e32 v13, v13, v11
	v_add_f32_e32 v13, v13, v12
	v_add_f32_e32 v13, v13, v15
	v_add_f32_e32 v13, v13, v50
	v_add_f32_e32 v13, v13, v51
	v_cvt_pk_bf16_f32 v10, v10, v11
	v_mfma_f32_32x32x16_bf16 v[34:49], v[6:9], v[66:69], v[34:49]
	v_cvt_pk_bf16_f32 v11, v12, v15
	v_cvt_pk_bf16_f32 v12, v50, v51
	s_waitcnt lgkmcnt(0)
	v_mfma_f32_32x32x16_bf16 v[18:33], v[6:9], v[74:77], v[18:33]
	v_fmamk_f32 v6, v122, 0x3e38aa3b, v14
	v_exp_f32_e32 v89, v6
	v_fmamk_f32 v6, v123, 0x3e38aa3b, v14
	v_exp_f32_e32 v94, v6
	v_fmamk_f32 v7, v124, 0x3e38aa3b, v14
	v_add_f32_e32 v6, v13, v52
	v_exp_f32_e32 v95, v7
	v_fmamk_f32 v7, v125, 0x3e38aa3b, v14
	v_add_f32_e32 v6, v6, v53
	v_exp_f32_e32 v96, v7
	v_fmamk_f32 v7, v126, 0x3e38aa3b, v14
	v_add_f32_e32 v6, v6, v89
	v_exp_f32_e32 v97, v7
	v_fmamk_f32 v7, v127, 0x3e38aa3b, v14
	v_add_f32_e32 v6, v6, v94
	v_exp_f32_e32 v114, v7
	v_fmamk_f32 v7, v128, 0x3e38aa3b, v14
	v_add_f32_e32 v6, v6, v95
	v_exp_f32_e32 v115, v7
	v_fmamk_f32 v7, v129, 0x3e38aa3b, v14
	v_add_f32_e32 v6, v6, v96
	v_exp_f32_e32 v116, v7
	v_fmamk_f32 v7, v98, 0x3e38aa3b, v14
	v_add_f32_e32 v6, v6, v97
	v_exp_f32_e32 v98, v7
	v_fmamk_f32 v7, v99, 0x3e38aa3b, v14
	v_add_f32_e32 v6, v6, v114
	v_exp_f32_e32 v99, v7
	v_fmamk_f32 v7, v100, 0x3e38aa3b, v14
	v_add_f32_e32 v6, v6, v115
	v_exp_f32_e32 v100, v7
	v_fmamk_f32 v7, v101, 0x3e38aa3b, v14
	v_add_f32_e32 v6, v6, v116
	v_exp_f32_e32 v101, v7
	v_fmamk_f32 v7, v102, 0x3e38aa3b, v14
	v_add_f32_e32 v6, v6, v98
	v_exp_f32_e32 v102, v7
	v_fmamk_f32 v7, v103, 0x3e38aa3b, v14
	v_add_f32_e32 v6, v6, v99
	v_exp_f32_e32 v103, v7
	v_add_f32_e32 v6, v6, v100
	v_add_f32_e32 v6, v6, v101
	v_add_f32_e32 v6, v6, v102
	v_add_f32_e32 v54, v6, v103
	v_fmamk_f32 v6, v104, 0x3e38aa3b, v14
	v_exp_f32_e32 v104, v6
	ds_read_b128 v[6:9], v250 offset:16384
	v_fmamk_f32 v13, v105, 0x3e38aa3b, v14
	v_exp_f32_e32 v105, v13
	v_cvt_pk_bf16_f32 v13, v52, v53
	ds_read_b128 v[50:53], v250 offset:18432
	ds_read_b128 v[90:93], v250 offset:17408
	ds_read_b128 v[118:121], v250 offset:19456
	ds_read_b128 v[122:125], v250 offset:20480
	ds_read_b128 v[126:129], v250 offset:22528
	s_waitcnt lgkmcnt(5)
	v_mfma_f32_32x32x16_bf16 v[66:81], v[6:9], v[10:13], 0
	v_add_f32_e32 v6, v54, v104
	v_add_f32_e32 v15, v6, v105
	v_fmamk_f32 v6, v106, 0x3e38aa3b, v14
	v_exp_f32_e32 v106, v6
	v_fmamk_f32 v6, v107, 0x3e38aa3b, v14
	v_exp_f32_e32 v107, v6
	s_waitcnt lgkmcnt(4)
	v_mfma_f32_32x32x16_bf16 v[50:65], v[50:53], v[10:13], 0
	v_fmamk_f32 v10, v108, 0x3e38aa3b, v14
	v_exp_f32_e32 v108, v10
	v_cvt_pk_bf16_f32 v10, v89, v94
	v_cvt_pk_bf16_f32 v11, v95, v96
	v_cvt_pk_bf16_f32 v12, v97, v114
	v_cvt_pk_bf16_f32 v13, v115, v116
	v_fmamk_f32 v94, v110, 0x3e38aa3b, v14
	v_exp_f32_e32 v89, v109
	s_waitcnt lgkmcnt(3)
	v_mfma_f32_32x32x16_bf16 v[66:81], v[90:93], v[10:13], v[66:81]
	v_exp_f32_e32 v109, v94
	v_add_f32_e32 v15, v15, v106
	v_add_f32_e32 v15, v15, v107
	v_add_f32_e32 v15, v15, v108
	v_add_f32_e32 v15, v15, v89
	v_add_f32_e32 v15, v15, v109
	s_waitcnt lgkmcnt(2)
	v_mfma_f32_32x32x16_bf16 v[50:65], v[118:121], v[10:13], v[50:65]
	v_cvt_pk_bf16_f32 v6, v98, v99
	v_cvt_pk_bf16_f32 v7, v100, v101
	v_cvt_pk_bf16_f32 v8, v102, v103
	v_cvt_pk_bf16_f32 v9, v104, v105
	ds_read_b128 v[94:97], v250 offset:21504
	s_waitcnt lgkmcnt(2)
	v_mfma_f32_32x32x16_bf16 v[66:81], v[122:125], v[6:9], v[66:81]
	v_fmamk_f32 v90, v111, 0x3e38aa3b, v14
	v_exp_f32_e32 v98, v90
	v_fmamk_f32 v90, v112, 0x3e38aa3b, v14
	v_fmac_f32_e32 v14, 0x3e38aa3b, v113
	v_exp_f32_e32 v99, v90
	ds_read_b128 v[90:93], v250 offset:23552
	v_add_f32_e32 v15, v15, v98
	s_waitcnt lgkmcnt(2)
	v_mfma_f32_32x32x16_bf16 v[50:65], v[126:129], v[6:9], v[50:65]
	v_exp_f32_e32 v11, v14
	v_add_f32_e32 v10, v15, v99
	v_cvt_pk_bf16_f32 v6, v106, v107
	v_cvt_pk_bf16_f32 v7, v108, v89
	v_cvt_pk_bf16_f32 v8, v109, v98
	v_cvt_pk_bf16_f32 v9, v99, v11
	v_add_f32_e32 v10, v10, v11
	v_mov_b32_e32 v11, v10
	s_waitcnt lgkmcnt(1)
	v_mfma_f32_32x32x16_bf16 v[66:81], v[94:97], v[6:9], v[66:81]
	v_permlane32_swap_b32_e32 v10, v11
	v_add_f32_e32 v10, v10, v11
	v_rcp_f32_e32 v101, v10
	v_cvt_pk_bf16_f32 v89, v16, v17
	v_ashrrev_i32_e32 v118, 3, v210
	v_and_b32_e32 v118, 0xffffffe0, v118
	v_bfe_u32 v119, v210, 6, 1
	v_add_u32_e32 v118, s16, v118
	v_lshl_or_b32 v118, v119, 4, v118
	v_or_b32_e32 v118, v118, v211
	v_lshlrev_b32_e32 v118, 10, v118
	v_add_u32_e32 v118, s2, v118
	v_bfe_u32 v119, v210, 7, 1
	v_lshl_or_b32 v118, v119, 5, v118
	v_or_b32_e32 v118, v118, v1
	v_lshlrev_b32_e32 v118, 2, v118
	global_load_dword v110, v118, s[12:13] sc1
	global_load_dword v111, v118, s[72:73] offset:-4096 sc1
	global_load_dword v112, v118, s[72:73] sc1
	global_load_dword v113, v118, s[76:77] offset:-4096 sc1
	global_load_dword v114, v118, s[76:77] sc1
	global_load_dword v115, v118, s[78:79] offset:-4096 sc1
	global_load_dword v116, v118, s[78:79] sc1
	global_load_dword v117, v118, s[74:75] sc1
	s_nop 6
	s_waitcnt vmcnt(32)
	v_fmac_f32_e32 v245, v101, v70
	s_waitcnt lgkmcnt(0)
	v_mfma_f32_32x32x16_bf16 v[50:65], v[90:93], v[6:9], v[50:65]
	v_fmac_f32_e32 v243, v101, v71
	v_fmac_f32_e32 v241, v101, v72
	v_fmac_f32_e32 v239, v101, v73
	global_store_dword v252, v245, s[58:59] nt
	global_store_dword v252, v243, s[58:59] offset:1024 nt
	global_store_dword v252, v241, s[58:59] offset:2048 nt
	global_store_dword v252, v239, s[58:59] offset:3072 nt
	v_max3_f32 v6, v34, s38, v35
	v_max3_f32 v6, v6, v36, v37
	v_max3_f32 v6, v6, v38, v39
	v_max3_f32 v6, v6, v40, v41
	v_max3_f32 v7, v18, s38, v19
	v_max3_f32 v6, v6, v42, v43
	v_max3_f32 v7, v7, v20, v21
	v_max3_f32 v6, v6, v44, v45
	v_max3_f32 v7, v7, v22, v23
	v_max3_f32 v6, v6, v46, v47
	v_max3_f32 v7, v7, v24, v25
	v_max3_f32 v6, v6, v48, v49
	v_max3_f32 v7, v7, v26, v27
	v_max3_f32 v7, v7, v28, v29
	v_mov_b32_e32 v8, v6
	s_waitcnt vmcnt(32)
	v_fmac_f32_e32 v244, v101, v74
	v_fmac_f32_e32 v242, v101, v75
	v_fmac_f32_e32 v240, v101, v76
	v_fmac_f32_e32 v238, v101, v77
	global_store_dword v252, v244, s[60:61] nt
	global_store_dword v252, v242, s[60:61] offset:1024 nt
	global_store_dword v252, v240, s[60:61] offset:2048 nt
	global_store_dword v252, v238, s[60:61] offset:3072 nt
	v_max3_f32 v7, v7, v30, v31
	s_nop 0
	v_permlane32_swap_b32_e32 v6, v8
	v_max3_f32 v7, v7, v32, v33
	v_max_f32_e32 v8, v8, v8
	v_max_f32_e32 v6, v6, v6
	v_max_f32_e32 v90, v6, v8
	v_mov_b32_e32 v6, v7
	s_nop 1
	v_permlane32_swap_b32_e32 v7, v6
	v_mul_f32_e32 v8, 0xbe38aa3b, v90
	v_fmamk_f32 v9, v34, 0x3e38aa3b, v8
	v_max_f32_e32 v6, v6, v6
	v_max_f32_e32 v7, v7, v7
	v_exp_f32_e32 v9, v9
	s_waitcnt vmcnt(30)
	v_fmac_f32_e32 v236, v101, v78
	v_fmac_f32_e32 v234, v101, v79
	v_fmac_f32_e32 v232, v101, v80
	v_fmac_f32_e32 v230, v101, v81
	global_store_dword v252, v236, s[62:63] nt
	global_store_dword v252, v234, s[62:63] offset:1024 nt
	global_store_dword v252, v232, s[62:63] offset:2048 nt
	global_store_dword v252, v230, s[62:63] offset:3072 nt
	v_max_f32_e32 v91, v7, v6
	v_fmamk_f32 v7, v35, 0x3e38aa3b, v8
	v_exp_f32_e32 v7, v7
	v_fmamk_f32 v10, v36, 0x3e38aa3b, v8
	v_exp_f32_e32 v10, v10
	v_fmamk_f32 v11, v37, 0x3e38aa3b, v8
	v_exp_f32_e32 v11, v11
	v_fmamk_f32 v12, v38, 0x3e38aa3b, v8
	v_add_f32_e32 v6, 0, v9
	v_exp_f32_e32 v12, v12
	v_fmamk_f32 v13, v39, 0x3e38aa3b, v8
	v_add_f32_e32 v6, v6, v7
	v_exp_f32_e32 v13, v13
	v_fmamk_f32 v14, v40, 0x3e38aa3b, v8
	v_add_f32_e32 v6, v6, v10
	s_waitcnt vmcnt(32)
	v_fmac_f32_e32 v237, v101, v50
	v_fmac_f32_e32 v235, v101, v51
	v_fmac_f32_e32 v233, v101, v52
	v_fmac_f32_e32 v231, v101, v53
	global_store_dword v252, v237, s[64:65] nt
	global_store_dword v252, v235, s[64:65] offset:1024 nt
	global_store_dword v252, v233, s[64:65] offset:2048 nt
	global_store_dword v252, v231, s[64:65] offset:3072 nt
	v_exp_f32_e32 v14, v14
	v_fmamk_f32 v15, v41, 0x3e38aa3b, v8
	v_fmamk_f32 v16, v42, 0x3e38aa3b, v8
	v_add_f32_e32 v6, v6, v11
	v_exp_f32_e32 v15, v15
	v_exp_f32_e32 v92, v16
	v_fmamk_f32 v16, v43, 0x3e38aa3b, v8
	v_add_f32_e32 v6, v6, v12
	v_exp_f32_e32 v93, v16
	v_fmamk_f32 v16, v44, 0x3e38aa3b, v8
	v_add_f32_e32 v6, v6, v13
	v_exp_f32_e32 v94, v16
	v_fmamk_f32 v16, v45, 0x3e38aa3b, v8
	v_add_f32_e32 v6, v6, v14
	v_exp_f32_e32 v95, v16
	s_waitcnt vmcnt(32)
	v_fmac_f32_e32 v228, v101, v54
	v_fmac_f32_e32 v226, v101, v55
	v_fmac_f32_e32 v224, v101, v56
	v_fmac_f32_e32 v222, v101, v57
	global_store_dword v252, v228, s[66:67] nt
	global_store_dword v252, v226, s[66:67] offset:1024 nt
	global_store_dword v252, v224, s[66:67] offset:2048 nt
	global_store_dword v252, v222, s[66:67] offset:3072 nt
	v_fmamk_f32 v16, v46, 0x3e38aa3b, v8
	v_add_f32_e32 v6, v6, v15
	v_exp_f32_e32 v96, v16
	v_fmamk_f32 v16, v47, 0x3e38aa3b, v8
	v_add_f32_e32 v6, v6, v92
	v_exp_f32_e32 v97, v16
	v_fmamk_f32 v16, v48, 0x3e38aa3b, v8
	v_add_f32_e32 v6, v6, v93
	v_exp_f32_e32 v98, v16
	v_fmac_f32_e32 v8, 0x3e38aa3b, v49
	v_mul_f32_e32 v16, 0xbe38aa3b, v91
	v_add_f32_e32 v6, v6, v94
	v_exp_f32_e32 v99, v8
	v_fmamk_f32 v8, v18, 0x3e38aa3b, v16
	v_add_f32_e32 v6, v6, v95
	v_fmac_f32_e32 v249, v101, v66
	v_fmac_f32_e32 v248, v101, v67
	v_fmac_f32_e32 v247, v101, v68
	v_fmac_f32_e32 v246, v101, v69
	global_store_dword v252, v249, s[4:5] nt
	global_store_dword v252, v248, s[4:5] offset:1024 nt
	global_store_dword v252, v247, s[4:5] offset:2048 nt
	global_store_dword v252, v246, s[4:5] offset:3072 nt
	v_exp_f32_e32 v17, v8
	v_fmamk_f32 v8, v19, 0x3e38aa3b, v16
	v_add_f32_e32 v6, v6, v96
	v_exp_f32_e32 v18, v8
	v_fmamk_f32 v8, v20, 0x3e38aa3b, v16
	v_add_f32_e32 v6, v6, v97
	v_exp_f32_e32 v19, v8
	v_fmamk_f32 v8, v21, 0x3e38aa3b, v16
	v_add_f32_e32 v6, v6, v98
	v_exp_f32_e32 v20, v8
	v_fmamk_f32 v8, v22, 0x3e38aa3b, v16
	v_add_f32_e32 v100, v6, v99
	v_add_f32_e32 v6, 0, v17
	v_exp_f32_e32 v21, v8
	s_waitcnt vmcnt(32)
	v_fmac_f32_e32 v221, v101, v62
	v_fmac_f32_e32 v220, v101, v63
	v_fmac_f32_e32 v219, v101, v64
	v_fmac_f32_e32 v218, v101, v65
	global_store_dword v252, v221, s[70:71] nt
	global_store_dword v252, v220, s[70:71] offset:1024 nt
	global_store_dword v252, v219, s[70:71] offset:2048 nt
	global_store_dword v252, v218, s[70:71] offset:3072 nt
	v_fmamk_f32 v8, v23, 0x3e38aa3b, v16
	v_add_f32_e32 v6, v6, v18
	v_exp_f32_e32 v22, v8
	v_fmamk_f32 v8, v24, 0x3e38aa3b, v16
	v_add_f32_e32 v6, v6, v19
	v_exp_f32_e32 v23, v8
	v_fmamk_f32 v8, v25, 0x3e38aa3b, v16
	v_add_f32_e32 v6, v6, v20
	v_exp_f32_e32 v24, v8
	v_fmamk_f32 v8, v26, 0x3e38aa3b, v16
	v_add_f32_e32 v6, v6, v21
	v_exp_f32_e32 v25, v8
	v_add_f32_e32 v6, v6, v22
	v_add_f32_e32 v6, v6, v23
	v_fmac_f32_e32 v229, v101, v58
	v_fmac_f32_e32 v227, v101, v59
	v_fmac_f32_e32 v225, v101, v60
	v_fmac_f32_e32 v223, v101, v61
	global_store_dword v252, v229, s[68:69] nt
	global_store_dword v252, v227, s[68:69] offset:1024 nt
	global_store_dword v252, v225, s[68:69] offset:2048 nt
	global_store_dword v252, v223, s[68:69] offset:3072 nt
	v_add_f32_e32 v6, v6, v24
	v_add_f32_e32 v26, v6, v25
	v_fmamk_f32 v6, v27, 0x3e38aa3b, v16
	v_exp_f32_e32 v27, v6
	v_cvt_pk_bf16_f32 v6, v9, v7
	v_cvt_pk_bf16_f32 v7, v10, v11
	v_fmamk_f32 v10, v28, 0x3e38aa3b, v16
	v_cvt_pk_bf16_f32 v9, v14, v15
	v_exp_f32_e32 v28, v10
	v_fmamk_f32 v14, v29, 0x3e38aa3b, v16
	v_cvt_pk_bf16_f32 v8, v12, v13
	v_cvt_pk_bf16_f32 v13, v23, v24
	v_exp_f32_e32 v23, v14
	v_fmamk_f32 v14, v30, 0x3e38aa3b, v16
	v_mfma_f32_32x32x16_bf16 v[66:81], v[202:205], v[6:9], 0
	v_exp_f32_e32 v24, v14
	v_add_f32_e32 v14, v26, v27
	v_add_f32_e32 v14, v14, v28
	v_add_f32_e32 v14, v14, v23
	v_cvt_pk_bf16_f32 v10, v17, v18
	v_cvt_pk_bf16_f32 v11, v19, v20
	v_cvt_pk_bf16_f32 v12, v21, v22
	v_mfma_f32_32x32x16_bf16 v[34:49], v[2:5], v[6:9], 0
	v_fmamk_f32 v6, v31, 0x3e38aa3b, v16
	v_exp_f32_e32 v26, v6
	v_add_f32_e32 v14, v14, v24
	v_fmamk_f32 v6, v32, 0x3e38aa3b, v16
	v_fmac_f32_e32 v16, 0x3e38aa3b, v33
	v_exp_f32_e32 v29, v6
	v_exp_f32_e32 v30, v16
	v_mfma_f32_32x32x16_bf16 v[50:65], v[202:205], v[10:13], 0
	v_add_f32_e32 v18, v14, v26
	v_mov_b32_e32 v22, v100
	s_nop 1
	v_permlane32_swap_b32_e32 v100, v22
	v_add_f32_e32 v32, v100, v22
	v_cvt_pk_bf16_f32 v22, v25, v27
	v_cvt_pk_bf16_f32 v23, v28, v23
	v_mfma_f32_32x32x16_bf16 v[2:17], v[2:5], v[10:13], 0
	v_cvt_pk_bf16_f32 v24, v24, v26
	v_cvt_pk_bf16_f32 v25, v29, v30
	v_lshlrev_b32_e32 v26, 2, v213
	v_lshl_or_b32 v27, v212, 10, v26
	v_add_f32_e32 v18, v18, v29
	v_add_u32_e32 v28, 0x10000, v27
	v_add_f32_e32 v31, v18, v30
	v_mfma_f32_32x32x16_bf16 v[2:17], v[86:89], v[22:25], v[2:17]
	ds_write_b32 v28, v90
	v_add_u32_e32 v28, 0x10100, v27
	v_cvt_pk_bf16_f32 v18, v92, v93
	v_cvt_pk_bf16_f32 v19, v94, v95
	v_cvt_pk_bf16_f32 v20, v96, v97
	v_cvt_pk_bf16_f32 v21, v98, v99
	ds_write_b32 v28, v32
	v_mov_b32_e32 v28, v31
	v_mfma_f32_32x32x16_bf16 v[66:81], v[82:85], v[18:21], v[66:81]
	s_nop 0
	v_permlane32_swap_b32_e32 v31, v28
	s_nop 0
	v_cvt_pk_bf16_f32 v2, v2, v3
	v_cvt_pk_bf16_f32 v3, v4, v5
	v_cvt_pk_bf16_f32 v4, v6, v7
	v_cvt_pk_bf16_f32 v5, v8, v9
	v_mfma_f32_32x32x16_bf16 v[34:49], v[86:89], v[18:21], v[34:49]
	v_add_u32_e32 v19, 0x10200, v27
	v_add_f32_e32 v18, v31, v28
	ds_write_b32 v19, v91
	v_add_u32_e32 v19, 0x10300, v27
	ds_write_b32 v19, v18
	v_cvt_pk_bf16_f32 v18, v66, v67
	v_cvt_pk_bf16_f32 v19, v68, v69
	v_mfma_f32_32x32x16_bf16 v[50:65], v[82:85], v[22:25], v[50:65]
	v_lshl_or_b32 v22, v212, 13, v206
	ds_write_b128 v22, v[2:5] offset:6144
	v_cvt_pk_bf16_f32 v2, v10, v11
	v_cvt_pk_bf16_f32 v3, v12, v13
	v_cvt_pk_bf16_f32 v4, v14, v15
	v_cvt_pk_bf16_f32 v5, v16, v17
	ds_write_b128 v22, v[2:5] offset:7168
	v_bfe_u32 v16, v210, 6, 1
	v_ashrrev_i32_e32 v14, 7, v210
	v_and_b32_e32 v15, 1, v14
	v_cvt_pk_bf16_f32 v20, v70, v71
	v_cvt_pk_bf16_f32 v21, v72, v73
	ds_write_b128 v22, v[18:21]
	v_cvt_pk_bf16_f32 v18, v74, v75
	v_cvt_pk_bf16_f32 v19, v76, v77
	v_cvt_pk_bf16_f32 v20, v78, v79
	v_cvt_pk_bf16_f32 v21, v80, v81
	ds_write_b128 v22, v[18:21] offset:1024
	v_cvt_pk_bf16_f32 v18, v50, v51
	v_cvt_pk_bf16_f32 v19, v52, v53
	v_cvt_pk_bf16_f32 v20, v54, v55
	v_cvt_pk_bf16_f32 v21, v56, v57
	ds_write_b128 v22, v[18:21] offset:2048
	v_cvt_pk_bf16_f32 v18, v58, v59
	v_cvt_pk_bf16_f32 v19, v60, v61
	v_cvt_pk_bf16_f32 v20, v62, v63
	v_cvt_pk_bf16_f32 v21, v64, v65
	ds_write_b128 v22, v[18:21] offset:3072
	v_cvt_pk_bf16_f32 v18, v34, v35
	v_cvt_pk_bf16_f32 v19, v36, v37
	v_cvt_pk_bf16_f32 v20, v38, v39
	v_cvt_pk_bf16_f32 v21, v40, v41
	ds_write_b128 v22, v[18:21] offset:4096
	v_cvt_pk_bf16_f32 v18, v42, v43
	v_cvt_pk_bf16_f32 v19, v44, v45
	v_cvt_pk_bf16_f32 v20, v46, v47
	v_cvt_pk_bf16_f32 v21, v48, v49
	ds_write_b128 v22, v[18:21] offset:5120
	v_lshl_or_b32 v4, v15, 9, v26
	v_or_b32_e32 v5, 0x10000, v4
	v_or_b32_e32 v12, 0x10d00, v4
	s_waitcnt lgkmcnt(0)
	s_barrier
	v_or_b32_e32 v6, 0x10100, v4
	v_or_b32_e32 v7, 0x10400, v4
	v_or_b32_e32 v8, 0x10500, v4
	v_or_b32_e32 v9, 0x10800, v4
	v_or_b32_e32 v10, 0x10900, v4
	v_or_b32_e32 v11, 0x10c00, v4
	ds_read_b32 v5, v5
	ds_read_b32 v13, v6
	ds_read_b32 v15, v7
	ds_read_b32 v24, v8
	ds_read_b32 v25, v9
	ds_read_b32 v26, v10
	ds_read_b32 v27, v11
	ds_read_b32 v12, v12
	v_or_b32_e32 v6, 0x11000, v4
	v_or_b32_e32 v7, 0x11100, v4
	v_or_b32_e32 v8, 0x11400, v4
	v_or_b32_e32 v9, 0x11500, v4
	v_or_b32_e32 v10, 0x11800, v4
	v_or_b32_e32 v11, 0x11900, v4
	v_or_b32_e32 v28, 0x11c00, v4
	v_or_b32_e32 v4, 0x11d00, v4
	ds_read_b32 v29, v6
	ds_read_b32 v30, v7
	ds_read_b32 v31, v8
	ds_read_b32 v32, v9
	ds_read_b32 v33, v10
	ds_read_b32 v34, v11
	ds_read_b32 v28, v28
	ds_read_b32 v35, v4
	v_lshlrev_b32_e32 v44, 11, v14
	v_lshlrev_b32_e32 v45, 10, v16
	v_or3_b32 v44, v206, v44, v45
	ds_read_b128 v[48:51], v44
	ds_read_b128 v[52:55], v44 offset:8192
	ds_read_b128 v[56:59], v44 offset:16384
	ds_read_b128 v[60:63], v44 offset:24576
	ds_read_b128 v[64:67], v44 offset:32768
	ds_read_b128 v[68:71], v44 offset:40960
	ds_read_b128 v[72:75], v44 offset:49152
	ds_read_b128 v[76:79], v44 offset:57344
	s_waitcnt lgkmcnt(8)
	v_max_f32_e32 v4, v15, v15
	v_max_f32_e32 v6, v5, v5
	v_max_f32_e32 v4, v6, v4
	v_max3_f32 v4, v4, v25, v27
	v_max3_f32 v4, v4, v29, v31
	v_max3_f32 v36, v4, v33, v28
	v_sub_f32_e32 v4, v5, v36
	v_mul_f32_e32 v4, 0x3e38aa3b, v4
	v_exp_f32_e32 v37, v4
	s_nop 0
	v_fma_f32 v13, v13, v37, 0
	s_waitcnt lgkmcnt(7)
	v_lshlrev_b32_e32 v16, 16, v48
	v_and_b32_e32 v4, 0xffff0000, v48
	v_fma_f32 v38, v37, v4, 0
	v_lshlrev_b32_e32 v4, 16, v49
	v_fma_f32 v39, v37, v4, 0
	v_and_b32_e32 v4, 0xffff0000, v49
	v_sub_f32_e32 v5, v15, v36
	v_fma_f32 v40, v37, v4, 0
	v_lshlrev_b32_e32 v4, 16, v50
	v_mul_f32_e32 v5, 0x3e38aa3b, v5
	v_fma_f32 v41, v37, v4, 0
	v_and_b32_e32 v4, 0xffff0000, v50
	v_exp_f32_e32 v15, v5
	v_fma_f32 v42, v37, v4, 0
	v_lshlrev_b32_e32 v4, 16, v51
	v_fma_f32 v43, v37, v4, 0
	v_and_b32_e32 v4, 0xffff0000, v51
	v_fma_f32 v16, v37, v16, 0
	v_fma_f32 v37, v37, v4, 0
	s_waitcnt lgkmcnt(6)
	v_lshlrev_b32_e32 v4, 16, v52
	v_fmac_f32_e32 v16, v15, v4
	v_and_b32_e32 v4, 0xffff0000, v52
	v_fmac_f32_e32 v38, v15, v4
	v_lshlrev_b32_e32 v4, 16, v53
	v_fmac_f32_e32 v39, v15, v4
	v_and_b32_e32 v4, 0xffff0000, v53
	v_fmac_f32_e32 v40, v15, v4
	v_lshlrev_b32_e32 v4, 16, v54
	v_fmac_f32_e32 v41, v15, v4
	v_and_b32_e32 v4, 0xffff0000, v54
	v_fmac_f32_e32 v42, v15, v4
	v_lshlrev_b32_e32 v4, 16, v55
	v_fmac_f32_e32 v43, v15, v4
	v_sub_f32_e32 v4, v25, v36
	v_mul_f32_e32 v4, 0x3e38aa3b, v4
	v_fmac_f32_e32 v13, v24, v15
	v_exp_f32_e32 v24, v4
	v_and_b32_e32 v8, 0xffff0000, v55
	v_fmac_f32_e32 v37, v15, v8
	v_fmac_f32_e32 v13, v26, v24
	s_waitcnt lgkmcnt(5)
	v_lshlrev_b32_e32 v15, 16, v56
	v_and_b32_e32 v4, 0xffff0000, v56
	v_fmac_f32_e32 v38, v24, v4
	v_lshlrev_b32_e32 v4, 16, v57
	v_fmac_f32_e32 v39, v24, v4
	v_and_b32_e32 v4, 0xffff0000, v57
	v_sub_f32_e32 v5, v27, v36
	v_fmac_f32_e32 v40, v24, v4
	v_lshlrev_b32_e32 v4, 16, v58
	v_mul_f32_e32 v5, 0x3e38aa3b, v5
	v_fmac_f32_e32 v16, v24, v15
	v_fmac_f32_e32 v41, v24, v4
	v_and_b32_e32 v4, 0xffff0000, v58
	v_exp_f32_e32 v15, v5
	v_fmac_f32_e32 v42, v24, v4
	v_lshlrev_b32_e32 v4, 16, v59
	v_fmac_f32_e32 v43, v24, v4
	v_and_b32_e32 v4, 0xffff0000, v59
	v_fmac_f32_e32 v37, v24, v4
	s_waitcnt lgkmcnt(4)
	v_lshlrev_b32_e32 v4, 16, v60
	v_fmac_f32_e32 v16, v15, v4
	v_and_b32_e32 v4, 0xffff0000, v60
	v_fmac_f32_e32 v38, v15, v4
	v_lshlrev_b32_e32 v4, 16, v61
	v_fmac_f32_e32 v39, v15, v4
	v_and_b32_e32 v4, 0xffff0000, v61
	v_fmac_f32_e32 v40, v15, v4
	v_lshlrev_b32_e32 v4, 16, v62
	v_fmac_f32_e32 v41, v15, v4
	v_and_b32_e32 v4, 0xffff0000, v62
	v_fmac_f32_e32 v42, v15, v4
	v_lshlrev_b32_e32 v4, 16, v63
	v_fmac_f32_e32 v43, v15, v4
	v_sub_f32_e32 v4, v29, v36
	v_mul_f32_e32 v4, 0x3e38aa3b, v4
	v_fmac_f32_e32 v13, v12, v15
	v_exp_f32_e32 v12, v4
	v_and_b32_e32 v8, 0xffff0000, v63
	v_fmac_f32_e32 v37, v15, v8
	v_fmac_f32_e32 v13, v30, v12
	s_waitcnt lgkmcnt(3)
	v_lshlrev_b32_e32 v15, 16, v64
	v_and_b32_e32 v4, 0xffff0000, v64
	v_fmac_f32_e32 v38, v12, v4
	v_lshlrev_b32_e32 v4, 16, v65
	v_fmac_f32_e32 v39, v12, v4
	v_and_b32_e32 v4, 0xffff0000, v65
	v_sub_f32_e32 v5, v31, v36
	v_fmac_f32_e32 v40, v12, v4
	v_lshlrev_b32_e32 v4, 16, v66
	v_mul_f32_e32 v5, 0x3e38aa3b, v5
	v_fmac_f32_e32 v16, v12, v15
	v_fmac_f32_e32 v41, v12, v4
	v_and_b32_e32 v4, 0xffff0000, v66
	v_exp_f32_e32 v15, v5
	v_fmac_f32_e32 v42, v12, v4
	v_lshlrev_b32_e32 v4, 16, v67
	v_fmac_f32_e32 v43, v12, v4
	v_and_b32_e32 v4, 0xffff0000, v67
	v_fmac_f32_e32 v37, v12, v4
	s_waitcnt lgkmcnt(2)
	v_lshlrev_b32_e32 v4, 16, v68
	v_fmac_f32_e32 v16, v15, v4
	v_and_b32_e32 v4, 0xffff0000, v68
	v_fmac_f32_e32 v38, v15, v4
	v_lshlrev_b32_e32 v4, 16, v69
	v_fmac_f32_e32 v39, v15, v4
	v_and_b32_e32 v4, 0xffff0000, v69
	v_fmac_f32_e32 v40, v15, v4
	v_lshlrev_b32_e32 v4, 16, v70
	v_fmac_f32_e32 v41, v15, v4
	v_and_b32_e32 v4, 0xffff0000, v70
	v_fmac_f32_e32 v42, v15, v4
	v_lshlrev_b32_e32 v4, 16, v71
	v_fmac_f32_e32 v43, v15, v4
	v_sub_f32_e32 v4, v33, v36
	v_mul_f32_e32 v4, 0x3e38aa3b, v4
	v_exp_f32_e32 v12, v4
	v_and_b32_e32 v8, 0xffff0000, v71
	v_fmac_f32_e32 v37, v15, v8
	v_fmac_f32_e32 v13, v32, v15
	s_waitcnt lgkmcnt(1)
	v_lshlrev_b32_e32 v14, 16, v72
	v_and_b32_e32 v4, 0xffff0000, v72
	v_fmac_f32_e32 v38, v12, v4
	v_lshlrev_b32_e32 v4, 16, v73
	v_fmac_f32_e32 v39, v12, v4
	v_and_b32_e32 v4, 0xffff0000, v73
	v_sub_f32_e32 v5, v28, v36
	v_fmac_f32_e32 v40, v12, v4
	v_lshlrev_b32_e32 v4, 16, v74
	v_mul_f32_e32 v5, 0x3e38aa3b, v5
	v_fmac_f32_e32 v41, v12, v4
	v_and_b32_e32 v4, 0xffff0000, v74
	v_exp_f32_e32 v5, v5
	v_fmac_f32_e32 v42, v12, v4
	v_lshlrev_b32_e32 v4, 16, v75
	v_fmac_f32_e32 v43, v12, v4
	v_and_b32_e32 v4, 0xffff0000, v75
	v_fmac_f32_e32 v16, v12, v14
	v_fmac_f32_e32 v37, v12, v4
	s_waitcnt lgkmcnt(0)
	v_lshlrev_b32_e32 v4, 16, v76
	v_fmac_f32_e32 v16, v5, v4
	v_and_b32_e32 v4, 0xffff0000, v76
	v_fmac_f32_e32 v38, v5, v4
	v_lshlrev_b32_e32 v4, 16, v77
	v_fmac_f32_e32 v13, v34, v12
	v_fmac_f32_e32 v39, v5, v4
	v_and_b32_e32 v4, 0xffff0000, v77
	v_fmac_f32_e32 v13, v35, v5
	v_fmac_f32_e32 v40, v5, v4
	v_lshlrev_b32_e32 v4, 16, v78
	v_fmac_f32_e32 v41, v5, v4
	v_and_b32_e32 v4, 0xffff0000, v78
	v_rcp_f32_e32 v6, v13
	v_fmac_f32_e32 v42, v5, v4
	v_lshlrev_b32_e32 v4, 16, v79
	v_fmac_f32_e32 v43, v5, v4
	v_and_b32_e32 v4, 0xffff0000, v79
	v_fmac_f32_e32 v37, v5, v4
	s_waitcnt vmcnt(32)
	v_fmac_f32_e32 v111, v6, v38
	v_fmac_f32_e32 v112, v6, v39
	global_store_dword v118, v111, s[80:81] offset:-4096 nt
	global_store_dword v118, v112, s[80:81] nt
	v_fmac_f32_e32 v117, v6, v40
	global_store_dword v118, v117, s[82:83] nt
	v_fmac_f32_e32 v113, v6, v41
	global_store_dword v118, v113, s[84:85] offset:-4096 nt
	v_fmac_f32_e32 v114, v6, v42
	global_store_dword v118, v114, s[84:85] nt
	v_fmac_f32_e32 v110, v6, v16
	global_store_dword v118, v110, s[14:15] nt
	v_fmac_f32_e32 v115, v6, v43
	v_fmac_f32_e32 v116, v6, v37
	s_and_b64 vcc, exec, s[18:19]
	global_store_dword v118, v115, s[86:87] offset:-4096 nt
	global_store_dword v118, v116, s[86:87] nt
	s_barrier
	s_cbranch_vccnz .LBB3_144
.LBB3_142:
	s_lshl_b32 s2, s41, 5
	s_add_i32 s2, s2, s22
	s_xor_b64 s[18:19], s[20:21], -1
	s_lshr_b32 s20, s2, 3
	v_mov_b32_e32 v210, v0
	s_add_i32 s20, s20, s24
	s_add_i32 s2, s20, s25
	v_ashrrev_i32_e32 v212, 6, v210
	v_lshl_add_u32 v2, s2, 3, v212
	v_ashrrev_i32_e32 v3, 31, v2
	v_and_b32_e32 v213, 63, v210
	v_lshlrev_b64 v[2:3], 15, v[2:3]
	v_lshl_add_u64 v[2:3], s[10:11], 0, v[2:3]
	v_lshlrev_b32_e32 v206, 4, v213
	v_lshl_add_u64 v[204:205], v[2:3], 0, v[206:207]
	v_and_b32_e32 v2, 3, v212
	v_lshlrev_b32_e32 v3, 3, v212
	v_and_or_b32 v214, v3, 32, v2
	v_and_b32_e32 v2, 0x3fffff8, v212
	v_add_u32_e32 v4, 8, v212
	v_or_b32_e32 v2, s23, v2
	v_and_b32_e32 v4, 0x3fffff8, v4
	v_or_b32_e32 v6, 8, v214
	v_lshlrev_b32_e32 v215, 6, v2
	v_or_b32_e32 v4, s23, v4
	v_or_b32_e32 v2, v6, v215
	v_lshlrev_b32_e32 v216, 6, v4
	v_lshlrev_b32_e32 v209, 10, v212
	v_ashrrev_i32_e32 v3, 31, v2
	v_or_b32_e32 v4, v216, v6
	v_or_b32_e32 v208, v206, v209
	v_lshl_add_u64 v[202:203], s[0:1], 0, v[206:207]
	v_lshlrev_b64 v[2:3], 10, v[2:3]
	v_ashrrev_i32_e32 v5, 31, v4
	s_waitcnt vmcnt(17)
	ds_write_b128 v208, v[190:193]
	s_waitcnt vmcnt(16)
	ds_write_b128 v208, v[194:197] offset:8192
	s_waitcnt vmcnt(15)
	ds_write_b128 v208, v[198:201] offset:16384
	v_lshl_add_u64 v[2:3], v[202:203], 0, v[2:3]
	v_lshlrev_b64 v[4:5], 10, v[4:5]
	v_lshl_add_u64 v[4:5], v[202:203], 0, v[4:5]
	global_load_dwordx4 v[98:101], v[2:3], off
	global_load_dwordx4 v[102:105], v[4:5], off
	v_add_u32_e32 v2, 16, v212
	v_and_b32_e32 v2, 0x3fffff8, v2
	v_or_b32_e32 v2, s23, v2
	v_lshlrev_b32_e32 v217, 6, v2
	v_or_b32_e32 v2, v217, v6
	v_ashrrev_i32_e32 v3, 31, v2
	v_lshlrev_b64 v[2:3], 10, v[2:3]
	v_lshl_add_u64 v[2:3], v[202:203], 0, v[2:3]
	global_load_dwordx4 v[106:109], v[2:3], off
	v_lshrrev_b32_e32 v2, 3, v210
	v_or_b32_e32 v10, 12, v214
	v_and_b32_e32 v211, 4, v2
	v_or_b32_e32 v2, v10, v215
	v_ashrrev_i32_e32 v3, 31, v2
	v_or_b32_e32 v4, v10, v216
	v_lshlrev_b64 v[2:3], 10, v[2:3]
	v_ashrrev_i32_e32 v5, 31, v4
	v_lshl_add_u64 v[2:3], v[202:203], 0, v[2:3]
	v_lshlrev_b64 v[4:5], 10, v[4:5]
	s_waitcnt lgkmcnt(0)
	s_barrier
	v_lshl_add_u64 v[4:5], v[202:203], 0, v[4:5]
	global_load_dwordx4 v[118:121], v[2:3], off
	global_load_dwordx4 v[122:125], v[4:5], off
	v_or_b32_e32 v2, v10, v217
	v_ashrrev_i32_e32 v3, 31, v2
	v_lshlrev_b64 v[2:3], 10, v[2:3]
	v_lshl_add_u64 v[2:3], v[202:203], 0, v[2:3]
	global_load_dwordx4 v[190:193], v[2:3], off
	v_lshlrev_b32_e32 v7, 2, v211
	v_or_b32_e32 v8, 0x1e000, v7
	v_or_b32_e32 v2, 0x1e040, v7
	v_or_b32_e32 v9, 0x1e020, v7
	ds_read_b128 v[50:53], v8
	ds_read_b128 v[54:57], v9
	v_or_b32_e32 v3, 0x1e060, v7
	ds_read_b128 v[58:61], v2
	ds_read_b128 v[62:65], v3
	v_or_b32_e32 v2, 0x1e080, v7
	v_or_b32_e32 v3, 0x1e0a0, v7
	ds_read_b128 v[18:21], v2
	ds_read_b128 v[22:25], v3
	v_or_b32_e32 v2, 0x1e0c0, v7
	v_or_b32_e32 v3, 0x1e0e0, v7
	ds_read_b128 v[26:29], v2
	ds_read_b128 v[30:33], v3
	v_or_b32_e32 v2, 0x1e100, v7
	v_and_b32_e32 v1, 31, v210
	v_or_b32_e32 v3, 0x1e120, v7
	ds_read_b128 v[82:85], v2
	ds_read_b128 v[86:89], v3
	v_or_b32_e32 v2, 0x1e140, v7
	v_lshlrev_b32_e32 v6, 2, v1
	v_or_b32_e32 v3, 0x1e160, v7
	ds_read_b128 v[90:93], v2
	ds_read_b128 v[94:97], v3
	v_or_b32_e32 v2, 0x1e180, v7
	v_or_b32_e32 v3, 0x1e1a0, v7
	ds_read_b128 v[34:37], v2
	ds_read_b128 v[38:41], v3
	v_or_b32_e32 v2, 0x1e1c0, v7
	v_or_b32_e32 v4, 0x1e200, v6
	v_or_b32_e32 v3, 0x1e1e0, v7
	ds_read_b32 v66, v4
	ds_read_b128 v[42:45], v2
	ds_read_b128 v[46:49], v3
	v_or_b32_e32 v2, 0x1e280, v6
	ds_read_b32 v2, v2
	ds_read_b128 v[110:113], v206
	ds_read_b128 v[114:117], v206 offset:4096
	ds_read_b128 v[126:129], v206 offset:8192
	ds_read_b128 v[194:197], v206 offset:12288
	ds_read_b128 v[198:201], v206 offset:16384
	ds_read_b128 v[218:221], v206 offset:20480
	s_waitcnt vmcnt(20)
	ds_write_b128 v208, v[174:177] offset:24576
	s_waitcnt vmcnt(19)
	ds_write_b128 v208, v[182:185] offset:32768
	s_waitcnt vmcnt(18)
	ds_write_b128 v208, v[186:189] offset:40960
	ds_read_b128 v[174:177], v206 offset:1024
	ds_read_b128 v[182:185], v206 offset:5120
	ds_read_b128 v[186:189], v206 offset:9216
	ds_read_b128 v[222:225], v206 offset:13312
	ds_read_b128 v[226:229], v206 offset:17408
	ds_read_b128 v[230:233], v206 offset:21504
	s_waitcnt lgkmcnt(14)
	v_mov_b32_e32 v67, v66
	v_mov_b32_e32 v68, v66
	v_mov_b32_e32 v69, v66
	v_mov_b32_e32 v70, v66
	v_mov_b32_e32 v71, v66
	v_mov_b32_e32 v72, v66
	v_mov_b32_e32 v73, v66
	v_mov_b32_e32 v74, v66
	v_mov_b32_e32 v75, v66
	v_mov_b32_e32 v76, v66
	v_mov_b32_e32 v77, v66
	v_mov_b32_e32 v78, v66
	v_mov_b32_e32 v79, v66
	v_mov_b32_e32 v80, v66
	v_mov_b32_e32 v81, v66
	v_mov_b32_e32 v3, v2
	v_mov_b32_e32 v4, v2
	v_mov_b32_e32 v5, v2
	v_mov_b32_e32 v6, v2
	v_mov_b32_e32 v7, v2
	v_mov_b32_e32 v8, v2
	v_mov_b32_e32 v9, v2
	v_mov_b32_e32 v10, v2
	v_mov_b32_e32 v11, v2
	v_mov_b32_e32 v12, v2
	v_mov_b32_e32 v13, v2
	v_mov_b32_e32 v14, v2
	v_mov_b32_e32 v15, v2
	v_mov_b32_e32 v16, v2
	v_mov_b32_e32 v17, v2
	s_waitcnt vmcnt(17)
	v_mfma_f32_32x32x16_bf16 v[50:65], v[110:113], v[170:173], v[50:65]
	s_waitcnt lgkmcnt(13)
	v_mfma_f32_32x32x16_bf16 v[18:33], v[114:117], v[170:173], v[18:33]
	s_waitcnt lgkmcnt(12)
	v_mfma_f32_32x32x16_bf16 v[82:97], v[126:129], v[170:173], v[82:97]
	s_waitcnt lgkmcnt(11)
	v_mfma_f32_32x32x16_bf16 v[34:49], v[194:197], v[170:173], v[34:49]
	s_waitcnt lgkmcnt(10)
	v_mfma_f32_32x32x16_bf16 v[66:81], v[170:173], v[198:201], v[66:81]
	s_waitcnt lgkmcnt(9)
	v_mfma_f32_32x32x16_bf16 v[2:17], v[170:173], v[218:221], v[2:17]
	ds_read_b128 v[110:113], v206 offset:2048
	ds_read_b128 v[114:117], v206 offset:6144
	ds_read_b128 v[126:129], v206 offset:10240
	ds_read_b128 v[170:173], v206 offset:14336
	ds_read_b128 v[194:197], v206 offset:18432
	ds_read_b128 v[198:201], v206 offset:22528
	s_waitcnt vmcnt(16) lgkmcnt(11)
	v_mfma_f32_32x32x16_bf16 v[50:65], v[174:177], v[162:165], v[50:65]
	s_waitcnt lgkmcnt(10)
	v_mfma_f32_32x32x16_bf16 v[18:33], v[182:185], v[162:165], v[18:33]
	s_waitcnt lgkmcnt(9)
	v_mfma_f32_32x32x16_bf16 v[82:97], v[186:189], v[162:165], v[82:97]
	s_waitcnt lgkmcnt(8)
	v_mfma_f32_32x32x16_bf16 v[34:49], v[222:225], v[162:165], v[34:49]
	s_waitcnt lgkmcnt(7)
	v_mfma_f32_32x32x16_bf16 v[66:81], v[162:165], v[226:229], v[66:81]
	s_waitcnt lgkmcnt(6)
	v_mfma_f32_32x32x16_bf16 v[2:17], v[162:165], v[230:233], v[2:17]
	s_waitcnt lgkmcnt(6)
	s_barrier
	ds_read_b128 v[162:165], v206 offset:3072
	ds_read_b128 v[174:177], v206 offset:7168
	ds_read_b128 v[182:185], v206 offset:11264
	ds_read_b128 v[186:189], v206 offset:15360
	ds_read_b128 v[218:221], v206 offset:19456
	ds_read_b128 v[222:225], v206 offset:23552
	s_waitcnt vmcnt(15) lgkmcnt(11)
	v_mfma_f32_32x32x16_bf16 v[50:65], v[110:113], v[154:157], v[50:65]
	s_waitcnt lgkmcnt(10)
	v_mfma_f32_32x32x16_bf16 v[18:33], v[114:117], v[154:157], v[18:33]
	s_waitcnt lgkmcnt(9)
	v_mfma_f32_32x32x16_bf16 v[82:97], v[126:129], v[154:157], v[82:97]
	s_waitcnt lgkmcnt(8)
	v_mfma_f32_32x32x16_bf16 v[34:49], v[170:173], v[154:157], v[34:49]
	s_waitcnt lgkmcnt(7)
	v_mfma_f32_32x32x16_bf16 v[66:81], v[154:157], v[194:197], v[66:81]
	s_waitcnt lgkmcnt(6)
	v_mfma_f32_32x32x16_bf16 v[2:17], v[154:157], v[198:201], v[2:17]
	ds_read_b128 v[194:197], v206 offset:24576
	ds_read_b128 v[198:201], v206 offset:28672
	ds_read_b128 v[226:229], v206 offset:32768
	ds_read_b128 v[230:233], v206 offset:36864
	ds_read_b128 v[234:237], v206 offset:40960
	ds_read_b128 v[238:241], v206 offset:45056
	v_add_co_u32_e32 v110, vcc, s29, v204
	s_waitcnt vmcnt(14) lgkmcnt(11)
	v_mfma_f32_32x32x16_bf16 v[50:65], v[162:165], v[146:149], v[50:65]
	v_addc_co_u32_e32 v111, vcc, 0, v205, vcc
	v_add_co_u32_e32 v242, vcc, s30, v204
	s_nop 1
	v_addc_co_u32_e32 v243, vcc, 0, v205, vcc
	global_load_dwordx4 v[126:129], v[110:111], off offset:1024
	global_load_dwordx4 v[114:117], v[110:111], off offset:2048
	global_load_dwordx4 v[154:157], v[242:243], off offset:-4096
	s_nop 0
	global_load_dwordx4 v[110:113], v[110:111], off offset:3072
	s_waitcnt lgkmcnt(10)
	v_mfma_f32_32x32x16_bf16 v[18:33], v[174:177], v[146:149], v[18:33]
	s_waitcnt lgkmcnt(9)
	v_mfma_f32_32x32x16_bf16 v[82:97], v[182:185], v[146:149], v[82:97]
	s_waitcnt lgkmcnt(8)
	v_mfma_f32_32x32x16_bf16 v[34:49], v[186:189], v[146:149], v[34:49]
	s_waitcnt lgkmcnt(7)
	v_mfma_f32_32x32x16_bf16 v[66:81], v[146:149], v[218:221], v[66:81]
	s_waitcnt lgkmcnt(6)
	v_mfma_f32_32x32x16_bf16 v[2:17], v[146:149], v[222:225], v[2:17]
	v_or_b32_e32 v170, 16, v214
	v_or_b32_e32 v146, v170, v215
	v_or_b32_e32 v148, v170, v216
	v_or_b32_e32 v170, v170, v217
	v_ashrrev_i32_e32 v147, 31, v146
	v_ashrrev_i32_e32 v149, 31, v148
	v_ashrrev_i32_e32 v171, 31, v170
	v_lshlrev_b64 v[146:147], 10, v[146:147]
	v_lshlrev_b64 v[148:149], 10, v[148:149]
	v_lshlrev_b64 v[170:171], 10, v[170:171]
	v_lshl_add_u64 v[146:147], v[202:203], 0, v[146:147]
	v_lshl_add_u64 v[162:163], v[202:203], 0, v[148:149]
	v_lshl_add_u64 v[170:171], v[202:203], 0, v[170:171]
	global_load_dwordx4 v[146:149], v[146:147], off
	s_nop 0
	global_load_dwordx4 v[162:165], v[162:163], off
	v_or_b32_e32 v244, 0x10000, v206
	global_load_dwordx4 v[170:173], v[170:171], off
	v_add_u32_e32 v209, v244, v209
	s_waitcnt vmcnt(12)
	ds_write_b128 v208, v[98:101] offset:49152
	s_waitcnt vmcnt(11)
	ds_write_b128 v208, v[102:105] offset:57344
	s_waitcnt vmcnt(10)
	ds_write_b128 v209, v[106:109]
	ds_read_b128 v[98:101], v206 offset:25600
	ds_read_b128 v[102:105], v206 offset:29696
	ds_read_b128 v[106:109], v206 offset:33792
	ds_read_b128 v[174:177], v206 offset:37888
	ds_read_b128 v[182:185], v206 offset:41984
	ds_read_b128 v[186:189], v206 offset:46080
	s_waitcnt lgkmcnt(14)
	v_mfma_f32_32x32x16_bf16 v[50:65], v[194:197], v[178:181], v[50:65]
	s_waitcnt lgkmcnt(13)
	v_mfma_f32_32x32x16_bf16 v[18:33], v[198:201], v[178:181], v[18:33]
	s_waitcnt lgkmcnt(12)
	v_mfma_f32_32x32x16_bf16 v[82:97], v[226:229], v[178:181], v[82:97]
	s_waitcnt lgkmcnt(11)
	v_mfma_f32_32x32x16_bf16 v[34:49], v[230:233], v[178:181], v[34:49]
	s_waitcnt lgkmcnt(10)
	v_mfma_f32_32x32x16_bf16 v[66:81], v[178:181], v[234:237], v[66:81]
	s_waitcnt lgkmcnt(9)
	v_mfma_f32_32x32x16_bf16 v[2:17], v[178:181], v[238:241], v[2:17]
	ds_read_b128 v[178:181], v206 offset:26624
	ds_read_b128 v[194:197], v206 offset:30720
	ds_read_b128 v[198:201], v206 offset:34816
	ds_read_b128 v[218:221], v206 offset:38912
	ds_read_b128 v[222:225], v206 offset:43008
	ds_read_b128 v[226:229], v206 offset:47104
	s_waitcnt lgkmcnt(11)
	v_mfma_f32_32x32x16_bf16 v[50:65], v[98:101], v[166:169], v[50:65]
	s_waitcnt lgkmcnt(10)
	v_mfma_f32_32x32x16_bf16 v[18:33], v[102:105], v[166:169], v[18:33]
	s_waitcnt lgkmcnt(9)
	v_mfma_f32_32x32x16_bf16 v[82:97], v[106:109], v[166:169], v[82:97]
	s_waitcnt lgkmcnt(8)
	v_mfma_f32_32x32x16_bf16 v[34:49], v[174:177], v[166:169], v[34:49]
	s_waitcnt lgkmcnt(7)
	v_mfma_f32_32x32x16_bf16 v[66:81], v[166:169], v[182:185], v[66:81]
	s_waitcnt lgkmcnt(6)
	v_mfma_f32_32x32x16_bf16 v[2:17], v[166:169], v[186:189], v[2:17]
	s_waitcnt lgkmcnt(6)
	s_barrier
	ds_read_b128 v[98:101], v206 offset:27648
	ds_read_b128 v[102:105], v206 offset:31744
	ds_read_b128 v[106:109], v206 offset:35840
	ds_read_b128 v[166:169], v206 offset:39936
	ds_read_b128 v[174:177], v206 offset:44032
	ds_read_b128 v[182:185], v206 offset:48128
	s_waitcnt lgkmcnt(11)
	v_mfma_f32_32x32x16_bf16 v[50:65], v[178:181], v[158:161], v[50:65]
	s_waitcnt lgkmcnt(10)
	v_mfma_f32_32x32x16_bf16 v[18:33], v[194:197], v[158:161], v[18:33]
	s_waitcnt lgkmcnt(9)
	v_mfma_f32_32x32x16_bf16 v[82:97], v[198:201], v[158:161], v[82:97]
	s_waitcnt lgkmcnt(8)
	v_mfma_f32_32x32x16_bf16 v[34:49], v[218:221], v[158:161], v[34:49]
	s_waitcnt lgkmcnt(7)
	v_mfma_f32_32x32x16_bf16 v[66:81], v[158:161], v[222:225], v[66:81]
	s_waitcnt lgkmcnt(6)
	v_mfma_f32_32x32x16_bf16 v[2:17], v[158:161], v[226:229], v[2:17]
	ds_read_b128 v[186:189], v206 offset:49152
	ds_read_b128 v[194:197], v206 offset:53248
	ds_read_b128 v[198:201], v206 offset:57344
	ds_read_b128 v[218:221], v206 offset:61440
	v_or_b32_e32 v240, 0x11000, v206
	ds_read_b128 v[222:225], v244
	ds_read_b128 v[226:229], v240
	s_waitcnt lgkmcnt(11)
	v_mfma_f32_32x32x16_bf16 v[50:65], v[98:101], v[150:153], v[50:65]
	s_waitcnt lgkmcnt(10)
	v_mfma_f32_32x32x16_bf16 v[18:33], v[102:105], v[150:153], v[18:33]
	s_waitcnt lgkmcnt(9)
	v_mfma_f32_32x32x16_bf16 v[82:97], v[106:109], v[150:153], v[82:97]
	global_load_dwordx4 v[158:161], v[242:243], off
	global_load_dwordx4 v[106:109], v[242:243], off offset:1024
	global_load_dwordx4 v[102:105], v[242:243], off offset:2048
	global_load_dwordx4 v[98:101], v[242:243], off offset:3072
	s_waitcnt lgkmcnt(8)
	v_mfma_f32_32x32x16_bf16 v[34:49], v[166:169], v[150:153], v[34:49]
	s_waitcnt lgkmcnt(7)
	v_mfma_f32_32x32x16_bf16 v[66:81], v[150:153], v[174:177], v[66:81]
	s_waitcnt lgkmcnt(6)
	v_mfma_f32_32x32x16_bf16 v[2:17], v[150:153], v[182:185], v[2:17]
	v_or_b32_e32 v174, 20, v214
	v_or_b32_e32 v150, v174, v215
	v_or_b32_e32 v152, v174, v216
	v_or_b32_e32 v174, v174, v217
	v_ashrrev_i32_e32 v151, 31, v150
	v_ashrrev_i32_e32 v153, 31, v152
	v_ashrrev_i32_e32 v175, 31, v174
	v_lshlrev_b64 v[150:151], 10, v[150:151]
	v_lshlrev_b64 v[152:153], 10, v[152:153]
	v_lshlrev_b64 v[174:175], 10, v[174:175]
	v_lshl_add_u64 v[150:151], v[202:203], 0, v[150:151]
	v_lshl_add_u64 v[166:167], v[202:203], 0, v[152:153]
	v_lshl_add_u64 v[174:175], v[202:203], 0, v[174:175]
	global_load_dwordx4 v[150:153], v[150:151], off
	s_nop 0
	global_load_dwordx4 v[166:169], v[166:167], off
	v_or_b32_e32 v241, 0x10400, v206
	global_load_dwordx4 v[178:181], v[174:175], off
	s_waitcnt vmcnt(16)
	ds_write_b128 v208, v[118:121]
	s_waitcnt vmcnt(15)
	ds_write_b128 v208, v[122:125] offset:8192
	s_waitcnt vmcnt(14)
	ds_write_b128 v208, v[190:193] offset:16384
	ds_read_b128 v[118:121], v206 offset:50176
	ds_read_b128 v[122:125], v206 offset:54272
	ds_read_b128 v[174:177], v206 offset:58368
	ds_read_b128 v[182:185], v206 offset:62464
	v_or_b32_e32 v242, 0x11400, v206
	ds_read_b128 v[190:193], v241
	ds_read_b128 v[230:233], v242
	s_waitcnt lgkmcnt(14)
	v_mfma_f32_32x32x16_bf16 v[50:65], v[186:189], v[142:145], v[50:65]
	s_waitcnt lgkmcnt(13)
	v_mfma_f32_32x32x16_bf16 v[18:33], v[194:197], v[142:145], v[18:33]
	s_waitcnt lgkmcnt(12)
	v_mfma_f32_32x32x16_bf16 v[82:97], v[198:201], v[142:145], v[82:97]
	s_waitcnt lgkmcnt(11)
	v_mfma_f32_32x32x16_bf16 v[34:49], v[218:221], v[142:145], v[34:49]
	s_waitcnt lgkmcnt(10)
	v_mfma_f32_32x32x16_bf16 v[66:81], v[142:145], v[222:225], v[66:81]
	s_waitcnt lgkmcnt(9)
	v_mfma_f32_32x32x16_bf16 v[2:17], v[142:145], v[226:229], v[2:17]
	ds_read_b128 v[142:145], v206 offset:51200
	ds_read_b128 v[186:189], v206 offset:55296
	ds_read_b128 v[194:197], v206 offset:59392
	ds_read_b128 v[198:201], v206 offset:63488
	v_or_b32_e32 v243, 0x10800, v206
	v_or_b32_e32 v245, 0x11800, v206
	ds_read_b128 v[218:221], v243
	ds_read_b128 v[222:225], v245
	s_waitcnt lgkmcnt(11)
	v_mfma_f32_32x32x16_bf16 v[50:65], v[118:121], v[138:141], v[50:65]
	s_waitcnt lgkmcnt(10)
	v_mfma_f32_32x32x16_bf16 v[18:33], v[122:125], v[138:141], v[18:33]
	s_waitcnt lgkmcnt(9)
	v_mfma_f32_32x32x16_bf16 v[82:97], v[174:177], v[138:141], v[82:97]
	s_waitcnt lgkmcnt(8)
	v_mfma_f32_32x32x16_bf16 v[34:49], v[182:185], v[138:141], v[34:49]
	s_waitcnt lgkmcnt(7)
	v_mfma_f32_32x32x16_bf16 v[66:81], v[138:141], v[190:193], v[66:81]
	s_waitcnt lgkmcnt(6)
	v_mfma_f32_32x32x16_bf16 v[2:17], v[138:141], v[230:233], v[2:17]
	s_waitcnt lgkmcnt(6)
	s_barrier
	ds_read_b128 v[118:121], v206 offset:52224
	ds_read_b128 v[122:125], v206 offset:56320
	ds_read_b128 v[138:141], v206 offset:60416
	ds_read_b128 v[174:177], v206 offset:64512
	v_or_b32_e32 v246, 0x10c00, v206
	v_or_b32_e32 v247, 0x11c00, v206
	ds_read_b128 v[182:185], v246
	ds_read_b128 v[190:193], v247
	s_waitcnt lgkmcnt(11)
	v_mfma_f32_32x32x16_bf16 v[50:65], v[142:145], v[134:137], v[50:65]
	s_waitcnt lgkmcnt(10)
	v_mfma_f32_32x32x16_bf16 v[18:33], v[186:189], v[134:137], v[18:33]
	s_waitcnt lgkmcnt(9)
	v_mfma_f32_32x32x16_bf16 v[82:97], v[194:197], v[134:137], v[82:97]
	s_waitcnt lgkmcnt(8)
	v_mfma_f32_32x32x16_bf16 v[34:49], v[198:201], v[134:137], v[34:49]
	s_waitcnt lgkmcnt(7)
	v_mfma_f32_32x32x16_bf16 v[66:81], v[134:137], v[218:221], v[66:81]
	s_waitcnt lgkmcnt(6)
	v_mfma_f32_32x32x16_bf16 v[2:17], v[134:137], v[222:225], v[2:17]
	ds_read_b128 v[186:189], v206
	ds_read_b128 v[218:221], v206 offset:4096
	ds_read_b128 v[222:225], v206 offset:8192
	ds_read_b128 v[226:229], v206 offset:12288
	ds_read_b128 v[230:233], v206 offset:16384
	ds_read_b128 v[234:237], v206 offset:20480
	s_waitcnt lgkmcnt(11)
	v_mfma_f32_32x32x16_bf16 v[50:65], v[118:121], v[130:133], v[50:65]
	v_add_co_u32_e32 v118, vcc, s31, v204
	s_nop 1
	v_addc_co_u32_e32 v119, vcc, 0, v205, vcc
	v_add_co_u32_e32 v238, vcc, s27, v204
	s_waitcnt lgkmcnt(10)
	v_mfma_f32_32x32x16_bf16 v[18:33], v[122:125], v[130:133], v[18:33]
	v_addc_co_u32_e32 v239, vcc, 0, v205, vcc
	s_waitcnt lgkmcnt(9)
	v_mfma_f32_32x32x16_bf16 v[82:97], v[138:141], v[130:133], v[82:97]
	global_load_dwordx4 v[138:141], v[118:119], off offset:1024
	global_load_dwordx4 v[134:137], v[118:119], off offset:2048
	s_waitcnt lgkmcnt(8)
	v_mfma_f32_32x32x16_bf16 v[34:49], v[174:177], v[130:133], v[34:49]
	s_waitcnt lgkmcnt(7)
	v_mfma_f32_32x32x16_bf16 v[66:81], v[130:133], v[182:185], v[66:81]
	s_waitcnt lgkmcnt(6)
	v_mfma_f32_32x32x16_bf16 v[2:17], v[130:133], v[190:193], v[2:17]
	global_load_dwordx4 v[142:145], v[238:239], off offset:-4096
	global_load_dwordx4 v[130:133], v[118:119], off offset:3072
	v_or_b32_e32 v122, 24, v214
	v_or_b32_e32 v118, v122, v215
	v_ashrrev_i32_e32 v119, 31, v118
	v_or_b32_e32 v120, v122, v216
	v_lshlrev_b64 v[118:119], 10, v[118:119]
	v_ashrrev_i32_e32 v121, 31, v120
	v_lshl_add_u64 v[118:119], v[202:203], 0, v[118:119]
	v_lshlrev_b64 v[120:121], 10, v[120:121]
	v_lshl_add_u64 v[120:121], v[202:203], 0, v[120:121]
	global_load_dwordx4 v[190:193], v[118:119], off
	global_load_dwordx4 v[194:197], v[120:121], off
	v_or_b32_e32 v118, v122, v217
	v_ashrrev_i32_e32 v119, 31, v118
	v_lshlrev_b64 v[118:119], 10, v[118:119]
	v_lshl_add_u64 v[118:119], v[202:203], 0, v[118:119]
	global_load_dwordx4 v[198:201], v[118:119], off
	s_waitcnt vmcnt(16)
	ds_write_b128 v208, v[146:149] offset:24576
	s_waitcnt vmcnt(15)
	ds_write_b128 v208, v[162:165] offset:32768
	s_waitcnt vmcnt(14)
	ds_write_b128 v208, v[170:173] offset:40960
	ds_read_b128 v[118:121], v206 offset:1024
	ds_read_b128 v[122:125], v206 offset:5120
	ds_read_b128 v[146:149], v206 offset:9216
	ds_read_b128 v[162:165], v206 offset:13312
	ds_read_b128 v[170:173], v206 offset:17408
	ds_read_b128 v[174:177], v206 offset:21504
	s_waitcnt lgkmcnt(14)
	v_mfma_f32_32x32x16_bf16 v[50:65], v[186:189], v[154:157], v[50:65]
	s_waitcnt lgkmcnt(13)
	v_mfma_f32_32x32x16_bf16 v[18:33], v[218:221], v[154:157], v[18:33]
	s_waitcnt lgkmcnt(12)
	v_mfma_f32_32x32x16_bf16 v[82:97], v[222:225], v[154:157], v[82:97]
	s_waitcnt lgkmcnt(11)
	v_mfma_f32_32x32x16_bf16 v[34:49], v[226:229], v[154:157], v[34:49]
	s_waitcnt lgkmcnt(10)
	v_mfma_f32_32x32x16_bf16 v[66:81], v[154:157], v[230:233], v[66:81]
	s_waitcnt lgkmcnt(9)
	v_mfma_f32_32x32x16_bf16 v[2:17], v[154:157], v[234:237], v[2:17]
	ds_read_b128 v[154:157], v206 offset:2048
	ds_read_b128 v[182:185], v206 offset:6144
	ds_read_b128 v[186:189], v206 offset:10240
	ds_read_b128 v[218:221], v206 offset:14336
	ds_read_b128 v[222:225], v206 offset:18432
	ds_read_b128 v[226:229], v206 offset:22528
	s_waitcnt lgkmcnt(11)
	v_mfma_f32_32x32x16_bf16 v[50:65], v[118:121], v[126:129], v[50:65]
	s_waitcnt lgkmcnt(10)
	v_mfma_f32_32x32x16_bf16 v[18:33], v[122:125], v[126:129], v[18:33]
	s_waitcnt lgkmcnt(9)
	v_mfma_f32_32x32x16_bf16 v[82:97], v[146:149], v[126:129], v[82:97]
	s_waitcnt lgkmcnt(8)
	v_mfma_f32_32x32x16_bf16 v[34:49], v[162:165], v[126:129], v[34:49]
	s_waitcnt lgkmcnt(7)
	v_mfma_f32_32x32x16_bf16 v[66:81], v[126:129], v[170:173], v[66:81]
	s_waitcnt lgkmcnt(6)
	v_mfma_f32_32x32x16_bf16 v[2:17], v[126:129], v[174:177], v[2:17]
	s_waitcnt lgkmcnt(6)
	s_barrier
	ds_read_b128 v[118:121], v206 offset:3072
	ds_read_b128 v[122:125], v206 offset:7168
	ds_read_b128 v[126:129], v206 offset:11264
	ds_read_b128 v[146:149], v206 offset:15360
	ds_read_b128 v[162:165], v206 offset:19456
	ds_read_b128 v[174:177], v206 offset:23552
	s_waitcnt lgkmcnt(11)
	v_mfma_f32_32x32x16_bf16 v[50:65], v[154:157], v[114:117], v[50:65]
	s_waitcnt lgkmcnt(10)
	v_mfma_f32_32x32x16_bf16 v[18:33], v[182:185], v[114:117], v[18:33]
	s_waitcnt lgkmcnt(9)
	v_mfma_f32_32x32x16_bf16 v[82:97], v[186:189], v[114:117], v[82:97]
	s_waitcnt lgkmcnt(8)
	v_mfma_f32_32x32x16_bf16 v[34:49], v[218:221], v[114:117], v[34:49]
	s_waitcnt lgkmcnt(7)
	v_mfma_f32_32x32x16_bf16 v[66:81], v[114:117], v[222:225], v[66:81]
	s_waitcnt lgkmcnt(6)
	v_mfma_f32_32x32x16_bf16 v[2:17], v[114:117], v[226:229], v[2:17]
	ds_read_b128 v[114:117], v206 offset:24576
	ds_read_b128 v[218:221], v206 offset:28672
	ds_read_b128 v[222:225], v206 offset:32768
	ds_read_b128 v[226:229], v206 offset:36864
	ds_read_b128 v[230:233], v206 offset:40960
	ds_read_b128 v[234:237], v206 offset:45056
	s_waitcnt lgkmcnt(8)
	v_mfma_f32_32x32x16_bf16 v[34:49], v[146:149], v[110:113], v[34:49]
	s_waitcnt lgkmcnt(7)
	v_mfma_f32_32x32x16_bf16 v[66:81], v[110:113], v[162:165], v[66:81]
	global_load_dwordx4 v[170:173], v[238:239], off
	global_load_dwordx4 v[162:165], v[238:239], off offset:1024
	global_load_dwordx4 v[154:157], v[238:239], off offset:2048
	global_load_dwordx4 v[146:149], v[238:239], off offset:3072
	v_mfma_f32_32x32x16_bf16 v[50:65], v[118:121], v[110:113], v[50:65]
	v_mfma_f32_32x32x16_bf16 v[18:33], v[122:125], v[110:113], v[18:33]
	v_mfma_f32_32x32x16_bf16 v[82:97], v[126:129], v[110:113], v[82:97]
	s_waitcnt lgkmcnt(6)
	v_mfma_f32_32x32x16_bf16 v[2:17], v[110:113], v[174:177], v[2:17]
	v_or_b32_e32 v118, 28, v214
	v_or_b32_e32 v110, v118, v215
	v_ashrrev_i32_e32 v111, 31, v110
	v_or_b32_e32 v112, v118, v216
	v_lshlrev_b64 v[110:111], 10, v[110:111]
	v_ashrrev_i32_e32 v113, 31, v112
	v_lshl_add_u64 v[110:111], v[202:203], 0, v[110:111]
	v_lshlrev_b64 v[112:113], 10, v[112:113]
	v_lshl_add_u64 v[112:113], v[202:203], 0, v[112:113]
	global_load_dwordx4 v[174:177], v[110:111], off
	global_load_dwordx4 v[182:185], v[112:113], off
	v_or_b32_e32 v110, v118, v217
	v_ashrrev_i32_e32 v111, 31, v110
	v_lshlrev_b64 v[110:111], 10, v[110:111]
	v_lshl_add_u64 v[110:111], v[202:203], 0, v[110:111]
	global_load_dwordx4 v[186:189], v[110:111], off
	s_waitcnt vmcnt(16)
	ds_write_b128 v208, v[150:153] offset:49152
	s_waitcnt vmcnt(15)
	ds_write_b128 v208, v[166:169] offset:57344
	s_waitcnt vmcnt(14)
	ds_write_b128 v209, v[178:181]
	ds_read_b128 v[110:113], v206 offset:25600
	ds_read_b128 v[118:121], v206 offset:29696
	ds_read_b128 v[122:125], v206 offset:33792
	ds_read_b128 v[126:129], v206 offset:37888
	ds_read_b128 v[150:153], v206 offset:41984
	ds_read_b128 v[166:169], v206 offset:46080
	s_waitcnt lgkmcnt(14)
	v_mfma_f32_32x32x16_bf16 v[50:65], v[114:117], v[158:161], v[50:65]
	s_waitcnt lgkmcnt(13)
	v_mfma_f32_32x32x16_bf16 v[18:33], v[218:221], v[158:161], v[18:33]
	s_waitcnt lgkmcnt(12)
	v_mfma_f32_32x32x16_bf16 v[82:97], v[222:225], v[158:161], v[82:97]
	s_waitcnt lgkmcnt(11)
	v_mfma_f32_32x32x16_bf16 v[34:49], v[226:229], v[158:161], v[34:49]
	s_waitcnt lgkmcnt(10)
	v_mfma_f32_32x32x16_bf16 v[66:81], v[158:161], v[230:233], v[66:81]
	s_waitcnt lgkmcnt(9)
	v_mfma_f32_32x32x16_bf16 v[2:17], v[158:161], v[234:237], v[2:17]
	ds_read_b128 v[114:117], v206 offset:26624
	ds_read_b128 v[158:161], v206 offset:30720
	ds_read_b128 v[178:181], v206 offset:34816
	ds_read_b128 v[218:221], v206 offset:38912
	ds_read_b128 v[222:225], v206 offset:43008
	ds_read_b128 v[226:229], v206 offset:47104
	s_waitcnt lgkmcnt(11)
	v_mfma_f32_32x32x16_bf16 v[50:65], v[110:113], v[106:109], v[50:65]
	s_waitcnt lgkmcnt(10)
	v_mfma_f32_32x32x16_bf16 v[18:33], v[118:121], v[106:109], v[18:33]
	s_waitcnt lgkmcnt(9)
	v_mfma_f32_32x32x16_bf16 v[82:97], v[122:125], v[106:109], v[82:97]
	s_waitcnt lgkmcnt(8)
	v_mfma_f32_32x32x16_bf16 v[34:49], v[126:129], v[106:109], v[34:49]
	s_waitcnt lgkmcnt(7)
	v_mfma_f32_32x32x16_bf16 v[66:81], v[106:109], v[150:153], v[66:81]
	s_waitcnt lgkmcnt(6)
	v_mfma_f32_32x32x16_bf16 v[2:17], v[106:109], v[166:169], v[2:17]
	s_waitcnt lgkmcnt(6)
	s_barrier
	ds_read_b128 v[106:109], v206 offset:27648
	ds_read_b128 v[110:113], v206 offset:31744
	ds_read_b128 v[118:121], v206 offset:35840
	ds_read_b128 v[122:125], v206 offset:39936
	ds_read_b128 v[126:129], v206 offset:44032
	ds_read_b128 v[230:233], v206 offset:48128
	s_waitcnt lgkmcnt(11)
	v_mfma_f32_32x32x16_bf16 v[50:65], v[114:117], v[102:105], v[50:65]
	s_waitcnt lgkmcnt(10)
	v_mfma_f32_32x32x16_bf16 v[18:33], v[158:161], v[102:105], v[18:33]
	s_waitcnt lgkmcnt(9)
	v_mfma_f32_32x32x16_bf16 v[82:97], v[178:181], v[102:105], v[82:97]
	s_waitcnt lgkmcnt(8)
	v_mfma_f32_32x32x16_bf16 v[34:49], v[218:221], v[102:105], v[34:49]
	s_waitcnt lgkmcnt(7)
	v_mfma_f32_32x32x16_bf16 v[66:81], v[102:105], v[222:225], v[66:81]
	s_waitcnt lgkmcnt(6)
	v_mfma_f32_32x32x16_bf16 v[2:17], v[102:105], v[226:229], v[2:17]
	ds_read_b128 v[102:105], v206 offset:49152
	ds_read_b128 v[114:117], v206 offset:53248
	ds_read_b128 v[218:221], v206 offset:57344
	ds_read_b128 v[222:225], v206 offset:61440
	ds_read_b128 v[226:229], v244
	ds_read_b128 v[234:237], v240
	s_waitcnt lgkmcnt(11)
	v_mfma_f32_32x32x16_bf16 v[50:65], v[106:109], v[98:101], v[50:65]
	v_add_co_u32_e32 v106, vcc, s33, v204
	s_nop 1
	v_addc_co_u32_e32 v107, vcc, 0, v205, vcc
	global_load_dwordx4 v[178:181], v[106:107], off
	global_load_dwordx4 v[166:169], v[106:107], off offset:1024
	global_load_dwordx4 v[158:161], v[106:107], off offset:2048
	global_load_dwordx4 v[150:153], v[106:107], off offset:3072
	s_waitcnt lgkmcnt(10)
	v_mfma_f32_32x32x16_bf16 v[18:33], v[110:113], v[98:101], v[18:33]
	s_waitcnt lgkmcnt(9)
	v_mfma_f32_32x32x16_bf16 v[82:97], v[118:121], v[98:101], v[82:97]
	s_waitcnt lgkmcnt(8)
	v_mfma_f32_32x32x16_bf16 v[34:49], v[122:125], v[98:101], v[34:49]
	s_waitcnt lgkmcnt(7)
	v_mfma_f32_32x32x16_bf16 v[66:81], v[98:101], v[126:129], v[66:81]
	s_waitcnt lgkmcnt(6)
	v_mfma_f32_32x32x16_bf16 v[2:17], v[98:101], v[230:233], v[2:17]
	s_waitcnt vmcnt(13)
	ds_write_b128 v208, v[190:193]
	s_waitcnt vmcnt(12)
	ds_write_b128 v208, v[194:197] offset:8192
	s_waitcnt vmcnt(11)
	ds_write_b128 v208, v[198:201] offset:16384
	ds_read_b128 v[98:101], v206 offset:50176
	ds_read_b128 v[106:109], v206 offset:54272
	ds_read_b128 v[110:113], v206 offset:58368
	ds_read_b128 v[118:121], v206 offset:62464
	ds_read_b128 v[122:125], v241
	ds_read_b128 v[126:129], v242
	s_waitcnt lgkmcnt(14)
	v_mfma_f32_32x32x16_bf16 v[50:65], v[102:105], v[142:145], v[50:65]
	s_waitcnt lgkmcnt(13)
	v_mfma_f32_32x32x16_bf16 v[18:33], v[114:117], v[142:145], v[18:33]
	s_waitcnt lgkmcnt(12)
	v_mfma_f32_32x32x16_bf16 v[82:97], v[218:221], v[142:145], v[82:97]
	s_waitcnt lgkmcnt(11)
	v_mfma_f32_32x32x16_bf16 v[34:49], v[222:225], v[142:145], v[34:49]
	s_waitcnt lgkmcnt(10)
	v_mfma_f32_32x32x16_bf16 v[66:81], v[142:145], v[226:229], v[66:81]
	s_waitcnt lgkmcnt(9)
	v_mfma_f32_32x32x16_bf16 v[2:17], v[142:145], v[234:237], v[2:17]
	ds_read_b128 v[102:105], v206 offset:51200
	ds_read_b128 v[114:117], v206 offset:55296
	ds_read_b128 v[218:221], v206 offset:59392
	ds_read_b128 v[222:225], v206 offset:63488
	ds_read_b128 v[226:229], v243
	ds_read_b128 v[230:233], v245
	s_waitcnt lgkmcnt(11)
	v_mfma_f32_32x32x16_bf16 v[50:65], v[98:101], v[138:141], v[50:65]
	s_waitcnt lgkmcnt(10)
	v_mfma_f32_32x32x16_bf16 v[18:33], v[106:109], v[138:141], v[18:33]
	s_waitcnt lgkmcnt(9)
	v_mfma_f32_32x32x16_bf16 v[82:97], v[110:113], v[138:141], v[82:97]
	s_waitcnt lgkmcnt(8)
	v_mfma_f32_32x32x16_bf16 v[34:49], v[118:121], v[138:141], v[34:49]
	s_waitcnt lgkmcnt(7)
	v_mfma_f32_32x32x16_bf16 v[66:81], v[138:141], v[122:125], v[66:81]
	s_waitcnt lgkmcnt(6)
	v_mfma_f32_32x32x16_bf16 v[2:17], v[138:141], v[126:129], v[2:17]
	s_waitcnt lgkmcnt(6)
	s_barrier
	ds_read_b128 v[98:101], v206 offset:52224
	ds_read_b128 v[106:109], v206 offset:56320
	ds_read_b128 v[110:113], v206 offset:60416
	ds_read_b128 v[118:121], v206 offset:64512
	ds_read_b128 v[122:125], v246
	ds_read_b128 v[126:129], v247
	s_waitcnt lgkmcnt(11)
	v_mfma_f32_32x32x16_bf16 v[50:65], v[102:105], v[134:137], v[50:65]
	s_waitcnt lgkmcnt(10)
	v_mfma_f32_32x32x16_bf16 v[18:33], v[114:117], v[134:137], v[18:33]
	s_waitcnt lgkmcnt(9)
	v_mfma_f32_32x32x16_bf16 v[82:97], v[218:221], v[134:137], v[82:97]
	s_waitcnt lgkmcnt(8)
	v_mfma_f32_32x32x16_bf16 v[34:49], v[222:225], v[134:137], v[34:49]
	s_waitcnt lgkmcnt(7)
	v_mfma_f32_32x32x16_bf16 v[66:81], v[134:137], v[226:229], v[66:81]
	s_waitcnt lgkmcnt(6)
	v_mfma_f32_32x32x16_bf16 v[2:17], v[134:137], v[230:233], v[2:17]
	ds_read_b128 v[102:105], v206
	ds_read_b128 v[114:117], v206 offset:4096
	ds_read_b128 v[218:221], v206 offset:8192
	ds_read_b128 v[222:225], v206 offset:12288
	ds_read_b128 v[226:229], v206 offset:16384
	ds_read_b128 v[230:233], v206 offset:20480
	s_waitcnt lgkmcnt(11)
	v_mfma_f32_32x32x16_bf16 v[50:65], v[98:101], v[130:133], v[50:65]
	s_waitcnt lgkmcnt(10)
	v_mfma_f32_32x32x16_bf16 v[18:33], v[106:109], v[130:133], v[18:33]
	s_waitcnt lgkmcnt(9)
	v_mfma_f32_32x32x16_bf16 v[82:97], v[110:113], v[130:133], v[82:97]
	s_waitcnt lgkmcnt(8)
	v_mfma_f32_32x32x16_bf16 v[34:49], v[118:121], v[130:133], v[34:49]
	s_waitcnt lgkmcnt(7)
	v_mfma_f32_32x32x16_bf16 v[66:81], v[130:133], v[122:125], v[66:81]
	s_waitcnt lgkmcnt(6)
	v_mfma_f32_32x32x16_bf16 v[2:17], v[130:133], v[126:129], v[2:17]
	s_waitcnt vmcnt(6)
	ds_write_b128 v208, v[174:177] offset:24576
	s_waitcnt vmcnt(5)
	ds_write_b128 v208, v[182:185] offset:32768
	s_waitcnt vmcnt(4)
	ds_write_b128 v208, v[186:189] offset:40960
	s_lshl_b64 s[42:43], s[2:3], 9
	s_or_b64 s[42:43], s[42:43], s[6:7]
	v_or_b32_e32 v252, s42, v211
	v_lshlrev_b32_e32 v252, 8, v252
	v_lshl_or_b32 v252, v212, 5, v252
	v_or_b32_e32 v252, v252, v1
	v_lshlrev_b32_e32 v252, 2, v252
	global_load_dword v249, v252, s[8:9] sc1
	global_load_dword v248, v252, s[8:9] offset:1024 sc1
	global_load_dword v247, v252, s[8:9] offset:2048 sc1
	global_load_dword v246, v252, s[8:9] offset:3072 sc1
	global_load_dword v245, v252, s[44:45] sc1
	global_load_dword v243, v252, s[44:45] offset:1024 sc1
	global_load_dword v241, v252, s[44:45] offset:2048 sc1
	global_load_dword v239, v252, s[44:45] offset:3072 sc1
	global_load_dword v244, v252, s[46:47] sc1
	global_load_dword v242, v252, s[46:47] offset:1024 sc1
	global_load_dword v240, v252, s[46:47] offset:2048 sc1
	global_load_dword v238, v252, s[46:47] offset:3072 sc1
	global_load_dword v236, v252, s[48:49] sc1
	global_load_dword v234, v252, s[48:49] offset:1024 sc1
	global_load_dword v237, v252, s[50:51] sc1
	global_load_dword v235, v252, s[50:51] offset:1024 sc1
	ds_read_b128 v[98:101], v206 offset:1024
	ds_read_b128 v[106:109], v206 offset:5120
	ds_read_b128 v[110:113], v206 offset:9216
	ds_read_b128 v[118:121], v206 offset:13312
	ds_read_b128 v[122:125], v206 offset:17408
	ds_read_b128 v[126:129], v206 offset:21504
	s_waitcnt lgkmcnt(14)
	v_mfma_f32_32x32x16_bf16 v[50:65], v[102:105], v[170:173], v[50:65]
	s_waitcnt lgkmcnt(13)
	v_mfma_f32_32x32x16_bf16 v[18:33], v[114:117], v[170:173], v[18:33]
	s_waitcnt lgkmcnt(12)
	v_mfma_f32_32x32x16_bf16 v[82:97], v[218:221], v[170:173], v[82:97]
	s_waitcnt lgkmcnt(11)
	v_mfma_f32_32x32x16_bf16 v[34:49], v[222:225], v[170:173], v[34:49]
	s_waitcnt lgkmcnt(10)
	v_mfma_f32_32x32x16_bf16 v[66:81], v[170:173], v[226:229], v[66:81]
	s_waitcnt lgkmcnt(9)
	v_mfma_f32_32x32x16_bf16 v[2:17], v[170:173], v[230:233], v[2:17]
	ds_read_b128 v[102:105], v206 offset:2048
	ds_read_b128 v[114:117], v206 offset:6144
	ds_read_b128 v[218:221], v206 offset:10240
	ds_read_b128 v[222:225], v206 offset:14336
	ds_read_b128 v[226:229], v206 offset:18432
	ds_read_b128 v[230:233], v206 offset:22528
	s_waitcnt lgkmcnt(11)
	v_mfma_f32_32x32x16_bf16 v[50:65], v[98:101], v[162:165], v[50:65]
	s_waitcnt lgkmcnt(10)
	v_mfma_f32_32x32x16_bf16 v[18:33], v[106:109], v[162:165], v[18:33]
	s_waitcnt lgkmcnt(9)
	v_mfma_f32_32x32x16_bf16 v[82:97], v[110:113], v[162:165], v[82:97]
	s_waitcnt lgkmcnt(8)
	v_mfma_f32_32x32x16_bf16 v[34:49], v[118:121], v[162:165], v[34:49]
	s_waitcnt lgkmcnt(7)
	v_mfma_f32_32x32x16_bf16 v[66:81], v[162:165], v[122:125], v[66:81]
	s_waitcnt lgkmcnt(6)
	v_mfma_f32_32x32x16_bf16 v[2:17], v[162:165], v[126:129], v[2:17]
	s_waitcnt lgkmcnt(6)
	s_barrier
	ds_read_b128 v[98:101], v206 offset:3072
	ds_read_b128 v[106:109], v206 offset:7168
	ds_read_b128 v[110:113], v206 offset:11264
	ds_read_b128 v[118:121], v206 offset:15360
	ds_read_b128 v[122:125], v206 offset:19456
	ds_read_b128 v[126:129], v206 offset:23552
	s_waitcnt lgkmcnt(11)
	v_mfma_f32_32x32x16_bf16 v[50:65], v[102:105], v[154:157], v[50:65]
	s_waitcnt lgkmcnt(10)
	v_mfma_f32_32x32x16_bf16 v[18:33], v[114:117], v[154:157], v[18:33]
	s_waitcnt lgkmcnt(9)
	v_mfma_f32_32x32x16_bf16 v[82:97], v[218:221], v[154:157], v[82:97]
	s_waitcnt lgkmcnt(8)
	v_mfma_f32_32x32x16_bf16 v[34:49], v[222:225], v[154:157], v[34:49]
	s_waitcnt lgkmcnt(7)
	v_mfma_f32_32x32x16_bf16 v[66:81], v[154:157], v[226:229], v[66:81]
	s_waitcnt lgkmcnt(6)
	v_mfma_f32_32x32x16_bf16 v[2:17], v[154:157], v[230:233], v[2:17]
	ds_read_b128 v[102:105], v206 offset:24576
	ds_read_b128 v[114:117], v206 offset:28672
	ds_read_b128 v[218:221], v206 offset:32768
	ds_read_b128 v[222:225], v206 offset:36864
	ds_read_b128 v[226:229], v206 offset:40960
	ds_read_b128 v[230:233], v206 offset:45056
	s_waitcnt lgkmcnt(11)
	v_mfma_f32_32x32x16_bf16 v[50:65], v[98:101], v[146:149], v[50:65]
	s_waitcnt lgkmcnt(10)
	v_mfma_f32_32x32x16_bf16 v[18:33], v[106:109], v[146:149], v[18:33]
	s_waitcnt lgkmcnt(9)
	v_mfma_f32_32x32x16_bf16 v[82:97], v[110:113], v[146:149], v[82:97]
	s_waitcnt lgkmcnt(8)
	v_mfma_f32_32x32x16_bf16 v[34:49], v[118:121], v[146:149], v[34:49]
	s_waitcnt lgkmcnt(7)
	v_mfma_f32_32x32x16_bf16 v[66:81], v[146:149], v[122:125], v[66:81]
	s_waitcnt lgkmcnt(6)
	v_mfma_f32_32x32x16_bf16 v[2:17], v[146:149], v[126:129], v[2:17]
	ds_read_b128 v[98:101], v206 offset:25600
	ds_read_b128 v[106:109], v206 offset:29696
	ds_read_b128 v[110:113], v206 offset:33792
	ds_read_b128 v[118:121], v206 offset:37888
	ds_read_b128 v[122:125], v206 offset:41984
	ds_read_b128 v[126:129], v206 offset:46080
	s_waitcnt vmcnt(19) lgkmcnt(11)
	v_mfma_f32_32x32x16_bf16 v[50:65], v[102:105], v[178:181], v[50:65]
	s_waitcnt lgkmcnt(10)
	v_mfma_f32_32x32x16_bf16 v[18:33], v[114:117], v[178:181], v[18:33]
	s_waitcnt lgkmcnt(9)
	v_mfma_f32_32x32x16_bf16 v[82:97], v[218:221], v[178:181], v[82:97]
	s_waitcnt lgkmcnt(8)
	v_mfma_f32_32x32x16_bf16 v[34:49], v[222:225], v[178:181], v[34:49]
	s_waitcnt lgkmcnt(7)
	v_mfma_f32_32x32x16_bf16 v[66:81], v[178:181], v[226:229], v[66:81]
	s_waitcnt lgkmcnt(6)
	v_mfma_f32_32x32x16_bf16 v[2:17], v[178:181], v[230:233], v[2:17]
	ds_read_b128 v[102:105], v206 offset:26624
	ds_read_b128 v[114:117], v206 offset:30720
	ds_read_b128 v[218:221], v206 offset:34816
	ds_read_b128 v[222:225], v206 offset:38912
	ds_read_b128 v[226:229], v206 offset:43008
	ds_read_b128 v[230:233], v206 offset:47104
	s_waitcnt vmcnt(18) lgkmcnt(11)
	v_mfma_f32_32x32x16_bf16 v[50:65], v[98:101], v[166:169], v[50:65]
	s_waitcnt lgkmcnt(10)
	v_mfma_f32_32x32x16_bf16 v[18:33], v[106:109], v[166:169], v[18:33]
	s_waitcnt lgkmcnt(9)
	v_mfma_f32_32x32x16_bf16 v[82:97], v[110:113], v[166:169], v[82:97]
	s_waitcnt lgkmcnt(8)
	v_mfma_f32_32x32x16_bf16 v[34:49], v[118:121], v[166:169], v[34:49]
	s_waitcnt lgkmcnt(7)
	v_mfma_f32_32x32x16_bf16 v[66:81], v[166:169], v[122:125], v[66:81]
	s_waitcnt lgkmcnt(6)
	v_mfma_f32_32x32x16_bf16 v[2:17], v[166:169], v[126:129], v[2:17]
	s_waitcnt lgkmcnt(6)
	s_barrier
	ds_read_b128 v[98:101], v206 offset:27648
	ds_read_b128 v[106:109], v206 offset:31744
	ds_read_b128 v[110:113], v206 offset:35840
	ds_read_b128 v[118:121], v206 offset:39936
	ds_read_b128 v[122:125], v206 offset:44032
	ds_read_b128 v[126:129], v206 offset:48128
	s_waitcnt vmcnt(17) lgkmcnt(11)
	v_mfma_f32_32x32x16_bf16 v[50:65], v[102:105], v[158:161], v[50:65]
	s_waitcnt lgkmcnt(10)
	v_mfma_f32_32x32x16_bf16 v[18:33], v[114:117], v[158:161], v[18:33]
	s_waitcnt lgkmcnt(9)
	v_mfma_f32_32x32x16_bf16 v[82:97], v[218:221], v[158:161], v[82:97]
	s_waitcnt lgkmcnt(8)
	v_mfma_f32_32x32x16_bf16 v[34:49], v[222:225], v[158:161], v[34:49]
	s_waitcnt lgkmcnt(7)
	v_mfma_f32_32x32x16_bf16 v[66:81], v[158:161], v[226:229], v[66:81]
	s_waitcnt lgkmcnt(6)
	v_mfma_f32_32x32x16_bf16 v[2:17], v[158:161], v[230:233], v[2:17]
	global_load_dword v232, v252, s[48:49] offset:2048 sc1
	global_load_dword v230, v252, s[48:49] offset:3072 sc1
	global_load_dword v233, v252, s[50:51] offset:2048 sc1
	global_load_dword v231, v252, s[50:51] offset:3072 sc1
	global_load_dword v228, v252, s[52:53] sc1
	global_load_dword v226, v252, s[52:53] offset:1024 sc1
	global_load_dword v224, v252, s[52:53] offset:2048 sc1
	global_load_dword v222, v252, s[52:53] offset:3072 sc1
	global_load_dword v229, v252, s[54:55] sc1
	global_load_dword v227, v252, s[54:55] offset:1024 sc1
	global_load_dword v225, v252, s[54:55] offset:2048 sc1
	global_load_dword v223, v252, s[54:55] offset:3072 sc1
	global_load_dword v221, v252, s[56:57] sc1
	global_load_dword v220, v252, s[56:57] offset:1024 sc1
	global_load_dword v219, v252, s[56:57] offset:2048 sc1
	global_load_dword v218, v252, s[56:57] offset:3072 sc1
	s_waitcnt vmcnt(32) lgkmcnt(5)
	v_mfma_f32_32x32x16_bf16 v[50:65], v[98:101], v[150:153], v[50:65]
	s_waitcnt lgkmcnt(4)
	v_mfma_f32_32x32x16_bf16 v[18:33], v[106:109], v[150:153], v[18:33]
	s_waitcnt lgkmcnt(3)
	v_mfma_f32_32x32x16_bf16 v[82:97], v[110:113], v[150:153], v[82:97]
	s_waitcnt lgkmcnt(2)
	v_mfma_f32_32x32x16_bf16 v[34:49], v[118:121], v[150:153], v[34:49]
	s_waitcnt lgkmcnt(1)
	v_mfma_f32_32x32x16_bf16 v[66:81], v[150:153], v[122:125], v[66:81]
	s_waitcnt lgkmcnt(0)
	v_mfma_f32_32x32x16_bf16 v[2:17], v[150:153], v[126:129], v[2:17]
	s_barrier
	s_and_b64 vcc, exec, s[18:19]
	s_cbranch_vccnz .LBB3_141
	v_or_b32_e32 v100, v215, v214
	v_ashrrev_i32_e32 v101, 31, v100
	v_or_b32_e32 v102, v216, v214
	v_lshlrev_b64 v[100:101], 10, v[100:101]
	v_ashrrev_i32_e32 v103, 31, v102
	v_lshl_add_u64 v[100:101], v[202:203], 0, v[100:101]
	v_lshlrev_b64 v[102:103], 10, v[102:103]
	v_lshl_add_u64 v[102:103], v[202:203], 0, v[102:103]
	global_load_dwordx4 v[190:193], v[100:101], off
	global_load_dwordx4 v[194:197], v[102:103], off
	v_or_b32_e32 v100, v217, v214
	v_or_b32_e32 v104, 4, v214
	v_ashrrev_i32_e32 v101, 31, v100
	v_or_b32_e32 v102, v104, v215
	v_lshlrev_b64 v[100:101], 10, v[100:101]
	v_ashrrev_i32_e32 v103, 31, v102
	v_add_u32_e32 v98, s28, v212
	v_lshl_add_u64 v[100:101], v[202:203], 0, v[100:101]
	v_lshlrev_b64 v[102:103], 10, v[102:103]
	v_ashrrev_i32_e32 v99, 31, v98
	v_lshl_add_u64 v[102:103], v[202:203], 0, v[102:103]
	global_load_dwordx4 v[198:201], v[100:101], off
	global_load_dwordx4 v[174:177], v[102:103], off
	v_or_b32_e32 v100, v216, v104
	v_lshlrev_b64 v[98:99], 15, v[98:99]
	v_ashrrev_i32_e32 v101, 31, v100
	v_or_b32_e32 v102, v217, v104
	v_lshl_add_u64 v[98:99], s[10:11], 0, v[98:99]
	v_lshlrev_b64 v[100:101], 10, v[100:101]
	v_ashrrev_i32_e32 v103, 31, v102
	v_lshl_add_u64 v[98:99], v[98:99], 0, v[206:207]
	v_lshl_add_u64 v[100:101], v[202:203], 0, v[100:101]
	v_lshlrev_b64 v[102:103], 10, v[102:103]
	v_lshl_add_u64 v[102:103], v[202:203], 0, v[102:103]
	global_load_dwordx4 v[182:185], v[100:101], off
	global_load_dwordx4 v[186:189], v[102:103], off
	global_load_dwordx4 v[170:173], v[98:99], off
	global_load_dwordx4 v[162:165], v[98:99], off offset:1024
	global_load_dwordx4 v[154:157], v[98:99], off offset:2048
	global_load_dwordx4 v[146:149], v[98:99], off offset:3072
	v_add_co_u32_e32 v100, vcc, 0x1000, v98
	s_nop 1
	v_addc_co_u32_e32 v101, vcc, 0, v99, vcc
	v_add_co_u32_e32 v98, vcc, 0x2000, v98
	global_load_dwordx4 v[178:181], v[100:101], off
	global_load_dwordx4 v[166:169], v[100:101], off offset:1024
	global_load_dwordx4 v[158:161], v[100:101], off offset:2048
	global_load_dwordx4 v[150:153], v[100:101], off offset:3072
	v_addc_co_u32_e32 v99, vcc, 0, v99, vcc
	global_load_dwordx4 v[142:145], v[98:99], off
	global_load_dwordx4 v[138:141], v[98:99], off offset:1024
	global_load_dwordx4 v[134:137], v[98:99], off offset:2048
	global_load_dwordx4 v[130:133], v[98:99], off offset:3072
	s_branch .LBB3_141
